# GEMM3 routing tail: the wave's 8 row-per-lane result stores are transposed through the dead LDS tile region and written as fully coalesced 1 KiB stores
# speedup vs baseline: 1.0201x; 1.0062x over previous
; #define PG8_LAS __attribute__((address_space(3)))
;     __device__ __forceinline__ void fused(f32x4 (&acc)[2][2][4][2], const Unit& u, int wr, int wc, int fr, int fq, PG8_LAS unsigned char* lds, int wid, int lane) const {
;     ...
;         if (half == 0) {
;             PG8_LAS int* idxl = (PG8_LAS int*)(lds + 65536) + row * 32;
;             float v0[16], v1[16];
; #pragma unroll
;             for (int q = 0; q < 16; ++q) { const unsigned b0 = __float_as_uint(top0[q]), b1 = __float_as_uint(top1[q]);
;                 v0[q] = __uint_as_float(b0 & ~127u); v1[q] = __uint_as_float(b1 & ~127u); idxl[q] = (int)(b0 & 127u); idxl[16 + q] = (int)(b1 & 127u); }
;             float best[16];
;             { float cv[16]; cv[0] = __uint_as_float((__float_as_uint(v0[0] + v1[0]) & ~255u) | 0u); cv[1] = __uint_as_float((__float_as_uint(v0[0] + v1[1]) & ~255u) | 1u); cv[2] = __uint_as_float((__float_as_uint(v0[0] + v1[2]) & ~255u) | 2u); cv[3] = __uint_as_float((__float_as_uint(v0[0] + v1[3]) & ~255u) | 3u); cv[4] = __uint_as_float((__float_as_uint(v0[0] + v1[4]) & ~255u) | 4u); cv[5] = __uint_as_float((__float_as_uint(v0[0] + v1[5]) & ~255u) | 5u); cv[6] = __uint_as_float((__float_as_uint(v0[0] + v1[6]) & ~255u) | 6u); cv[7] = __uint_as_float((__float_as_uint(v0[0] + v1[7]) & ~255u) | 7u); cv[8] = __uint_as_float((__float_as_uint(v0[0] + v1[8]) & ~255u) | 8u); cv[9] = __uint_as_float((__float_as_uint(v0[0] + v1[9]) & ~255u) | 9u); cv[10] = __uint_as_float((__float_as_uint(v0[0] + v1[10]) & ~255u) | 10u); cv[11] = __uint_as_float((__float_as_uint(v0[0] + v1[11]) & ~255u) | 11u); cv[12] = __uint_as_float((__float_as_uint(v0[0] + v1[12]) & ~255u) | 12u); cv[13] = __uint_as_float((__float_as_uint(v0[0] + v1[13]) & ~255u) | 13u); cv[14] = __uint_as_float((__float_as_uint(v0[0] + v1[14]) & ~255u) | 14u); cv[15] = __uint_as_float((__float_as_uint(v0[0] + v1[15]) & ~255u) | 15u); sort16_desc(cv);
; #pragma unroll
;               for (int q = 0; q < 16; ++q) best[q] = cv[q]; }
.LBB0_588:
	s_waitcnt lgkmcnt(0)
	s_barrier
	s_and_b64 vcc, exec, s[4:5]
	s_cbranch_vccnz .LBB0_590
	v_lshl_add_u32 v16, v128, 7, 0
	v_add_u32_e32 v16, 0x10000, v16
	v_and_b32_e32 v17, 0xffffff80, v12
	v_and_b32_e32 v18, 0xffffff80, v13
	v_and_b32_e32 v21, 0x7f, v77
	v_and_b32_e32 v20, 0x7f, v76
	v_and_b32_e32 v13, 0x7f, v13
	v_and_b32_e32 v12, 0x7f, v12
	v_and_b32_e32 v26, 0xffffff80, v14
	v_and_b32_e32 v28, 0xffffff80, v15
	v_and_b32_e32 v23, 0x7f, v79
	v_and_b32_e32 v22, 0x7f, v78
	v_and_b32_e32 v15, 0x7f, v15
	v_and_b32_e32 v14, 0x7f, v14
	ds_write_b128 v16, v[20:23]
	ds_write_b128 v16, v[12:15] offset:64
	v_and_b32_e32 v21, 0xffffff80, v8
	v_and_b32_e32 v23, 0xffffff80, v9
	v_and_b32_e32 v13, 0x7f, v73
	v_and_b32_e32 v12, 0x7f, v72
	v_and_b32_e32 v9, 0x7f, v9
	v_and_b32_e32 v8, 0x7f, v8
	v_and_b32_e32 v30, 0xffffff80, v10
	v_and_b32_e32 v32, 0xffffff80, v11
	v_and_b32_e32 v15, 0x7f, v75
	v_and_b32_e32 v14, 0x7f, v74
	v_and_b32_e32 v11, 0x7f, v11
	v_and_b32_e32 v10, 0x7f, v10
	v_and_b32_e32 v19, 0xffffff80, v76
	ds_write_b128 v16, v[12:15] offset:16
	ds_write_b128 v16, v[8:11] offset:80
	v_and_b32_e32 v13, 0xffffff80, v4
	v_and_b32_e32 v15, 0xffffff80, v5
	v_and_b32_e32 v9, 0x7f, v69
	v_and_b32_e32 v8, 0x7f, v68
	v_and_b32_e32 v5, 0x7f, v5
	v_and_b32_e32 v4, 0x7f, v4
	v_and_b32_e32 v34, 0xffffff80, v6
	v_and_b32_e32 v36, 0xffffff80, v7
	v_and_b32_e32 v11, 0x7f, v71
	v_and_b32_e32 v10, 0x7f, v70
	v_and_b32_e32 v7, 0x7f, v7
	v_and_b32_e32 v6, 0x7f, v6
	ds_write_b128 v16, v[8:11] offset:32
	ds_write_b128 v16, v[4:7] offset:96
	v_and_b32_e32 v5, 0x7f, v65
	v_and_b32_e32 v4, 0x7f, v64
	v_and_b32_e32 v41, 0xffffff80, v2
	v_and_b32_e32 v42, 0xffffff80, v3
	v_and_b32_e32 v7, 0x7f, v67
	v_and_b32_e32 v6, 0x7f, v66
	v_and_b32_e32 v11, 0x7f, v3
	v_and_b32_e32 v10, 0x7f, v2
	v_add_f32_e32 v2, v19, v17
	s_movk_i32 s4, 0xff00
	v_add_f32_e32 v3, v19, v18
	v_and_b32_e32 v24, 0xffffff80, v77
	ds_write_b128 v16, v[4:7] offset:48
	v_and_b32_e32 v2, 0xffffff00, v2
	v_and_or_b32 v3, v3, s4, 1
	v_add_f32_e32 v4, v19, v26
	v_add_f32_e32 v5, v19, v28
	v_and_b32_e32 v40, 0xffffff80, v1
	v_and_b32_e32 v9, 0x7f, v1
	v_and_b32_e32 v8, 0x7f, v0
	v_and_or_b32 v4, v4, s4, 2
	v_and_or_b32 v5, v5, s4, 3
	v_add_f32_e32 v48, v24, v17
	v_add_f32_e32 v49, v24, v18
	ds_write_b128 v16, v[8:11] offset:112
	v_add_f32_e32 v6, v19, v21
	v_add_f32_e32 v7, v19, v23
	v_add_f32_e32 v11, v19, v15
	v_add_f32_e32 v15, v19, v36
	v_add_f32_e32 v36, v19, v40
	v_max_f32_e32 v40, v2, v3
	v_min_f32_e32 v2, v2, v3
	v_max_f32_e32 v3, v5, v5
	v_and_or_b32 v48, v48, s4, 16
	v_and_or_b32 v49, v49, s4, 17
	v_add_f32_e32 v50, v24, v26
	v_add_f32_e32 v51, v24, v28
	v_and_or_b32 v6, v6, s4, 4
	v_and_or_b32 v7, v7, s4, 5
	v_add_f32_e32 v8, v19, v30
	v_add_f32_e32 v9, v19, v32
	v_max_f32_e32 v5, v4, v3
	v_min_f32_e32 v3, v4, v3
	v_and_or_b32 v50, v50, s4, 18
	v_and_or_b32 v51, v51, s4, 19
	v_and_or_b32 v8, v8, s4, 6
	v_and_or_b32 v9, v9, s4, 7
	v_max_f32_e32 v4, v40, v5
	v_min_f32_e32 v5, v40, v5
	v_max_f32_e32 v40, v2, v3
	v_add_f32_e32 v52, v24, v21
	v_add_f32_e32 v23, v24, v23
	v_add_f32_e32 v30, v24, v30
	v_add_f32_e32 v24, v24, v32
	v_max_f32_e32 v58, v48, v49
	v_min_f32_e32 v48, v48, v49
	v_max_f32_e32 v49, v51, v51
	v_min_f32_e32 v2, v2, v3
	v_max_f32_e32 v3, v40, v5
	v_min_f32_e32 v5, v40, v5
	v_max_f32_e32 v40, v6, v7
	v_min_f32_e32 v6, v6, v7
	v_max_f32_e32 v7, v9, v9
	v_and_or_b32 v52, v52, s4, 20
	v_and_or_b32 v23, v23, s4, 21
	v_and_or_b32 v30, v30, s4, 22
	v_and_or_b32 v24, v24, s4, 23
	v_max_f32_e32 v51, v50, v49
	v_min_f32_e32 v49, v50, v49
	v_max_f32_e32 v9, v8, v7
	v_min_f32_e32 v7, v8, v7
	v_max_f32_e32 v50, v58, v51
	v_min_f32_e32 v51, v58, v51
	v_max_f32_e32 v58, v48, v49
	v_max_f32_e32 v8, v40, v9
	v_min_f32_e32 v9, v40, v9
	v_max_f32_e32 v40, v6, v7
	v_min_f32_e32 v48, v48, v49
	v_max_f32_e32 v49, v58, v51
	v_min_f32_e32 v51, v58, v51
	v_max_f32_e32 v58, v52, v23
	v_min_f32_e32 v23, v52, v23
	v_max_f32_e32 v52, v30, v24
	v_min_f32_e32 v24, v30, v24
	v_min_f32_e32 v6, v6, v7
	v_max_f32_e32 v7, v40, v9
	v_min_f32_e32 v9, v40, v9
	v_max_f32_e32 v30, v58, v52
	v_min_f32_e32 v52, v58, v52
	v_max_f32_e32 v58, v23, v24
	v_max_f32_e32 v40, v4, v8
	v_min_f32_e32 v4, v4, v8
	v_max_f32_e32 v8, v5, v9
	v_min_f32_e32 v23, v23, v24
	v_max_f32_e32 v24, v58, v52
	v_min_f32_e32 v52, v58, v52
	v_and_b32_e32 v25, 0xffffff80, v78
	v_add_f32_e32 v10, v19, v13
	v_min_f32_e32 v5, v5, v9
	v_max_f32_e32 v9, v8, v4
	v_min_f32_e32 v4, v8, v4
	v_max_f32_e32 v8, v3, v7
	v_min_f32_e32 v3, v3, v7
	v_max_f32_e32 v7, v2, v6
	v_max_f32_e32 v58, v50, v30
	v_min_f32_e32 v30, v50, v30
	v_max_f32_e32 v50, v51, v52
	v_and_or_b32 v10, v10, s4, 8
	v_and_or_b32 v11, v11, s4, 9
	v_add_f32_e32 v13, v19, v34
	v_min_f32_e32 v2, v2, v6
	v_max_f32_e32 v6, v7, v3
	v_min_f32_e32 v3, v7, v3
	v_add_f32_e32 v32, v25, v17
	v_add_f32_e32 v53, v25, v18
	v_min_f32_e32 v51, v51, v52
	v_max_f32_e32 v52, v50, v30
	v_min_f32_e32 v30, v50, v30
	v_max_f32_e32 v50, v49, v24
	v_min_f32_e32 v24, v49, v24
	v_max_f32_e32 v49, v48, v23
	v_and_or_b32 v13, v13, s4, 10
	v_and_or_b32 v15, v15, s4, 11
	v_max_f32_e32 v7, v8, v9
	v_min_f32_e32 v8, v8, v9
	v_max_f32_e32 v9, v6, v4
	v_min_f32_e32 v4, v6, v4
	v_max_f32_e32 v6, v3, v5
	v_min_f32_e32 v3, v3, v5
	v_max_f32_e32 v5, v11, v11
	v_and_or_b32 v32, v32, s4, 32
	v_and_or_b32 v53, v53, s4, 33
	v_add_f32_e32 v54, v25, v26
	v_add_f32_e32 v55, v25, v28
	v_min_f32_e32 v23, v48, v23
	v_max_f32_e32 v48, v49, v24
	v_min_f32_e32 v24, v49, v24
	v_and_b32_e32 v27, 0xffffff80, v79
	v_and_b32_e32 v38, 0xffffff80, v0
	v_max_f32_e32 v11, v10, v5
	v_min_f32_e32 v5, v10, v5
	v_max_f32_e32 v10, v15, v15
;     __device__ __forceinline__ void fused(f32x4 (&acc)[2][2][4][2], const Unit& u, int wr, int wc, int fr, int fq, PG8_LAS unsigned char* lds, int wid, int lane) const {
;     ...
;             { float cv[16]; cv[0] = __uint_as_float((__float_as_uint(v0[0] + v1[0]) & ~255u) | 0u); cv[1] = __uint_as_float((__float_as_uint(v0[0] + v1[1]) & ~255u) | 1u); cv[2] = __uint_as_float((__float_as_uint(v0[0] + v1[2]) & ~255u) | 2u); cv[3] = __uint_as_float((__float_as_uint(v0[0] + v1[3]) & ~255u) | 3u); cv[4] = __uint_as_float((__float_as_uint(v0[0] + v1[4]) & ~255u) | 4u); cv[5] = __uint_as_float((__float_as_uint(v0[0] + v1[5]) & ~255u) | 5u); cv[6] = __uint_as_float((__float_as_uint(v0[0] + v1[6]) & ~255u) | 6u); cv[7] = __uint_as_float((__float_as_uint(v0[0] + v1[7]) & ~255u) | 7u); cv[8] = __uint_as_float((__float_as_uint(v0[0] + v1[8]) & ~255u) | 8u); cv[9] = __uint_as_float((__float_as_uint(v0[0] + v1[9]) & ~255u) | 9u); cv[10] = __uint_as_float((__float_as_uint(v0[0] + v1[10]) & ~255u) | 10u); cv[11] = __uint_as_float((__float_as_uint(v0[0] + v1[11]) & ~255u) | 11u); cv[12] = __uint_as_float((__float_as_uint(v0[0] + v1[12]) & ~255u) | 12u); cv[13] = __uint_as_float((__float_as_uint(v0[0] + v1[13]) & ~255u) | 13u); cv[14] = __uint_as_float((__float_as_uint(v0[0] + v1[14]) & ~255u) | 14u); cv[15] = __uint_as_float((__float_as_uint(v0[0] + v1[15]) & ~255u) | 15u); sort16_desc(cv);
; #pragma unroll
;               for (int q = 0; q < 16; ++q) best[q] = cv[q]; }
	v_and_or_b32 v54, v54, s4, 34
	v_and_or_b32 v55, v55, s4, 35
	v_max_f32_e32 v49, v50, v52
	v_min_f32_e32 v50, v50, v52
	v_max_f32_e32 v52, v48, v30
	v_min_f32_e32 v30, v48, v30
	v_max_f32_e32 v48, v24, v51
	v_min_f32_e32 v24, v24, v51
	v_max_f32_e32 v51, v53, v53
	v_add_f32_e32 v34, v19, v38
	v_max_f32_e32 v15, v13, v10
	v_min_f32_e32 v10, v13, v10
	v_add_f32_e32 v21, v25, v21
	v_add_f32_e32 v25, v27, v17
	v_max_f32_e32 v53, v32, v51
	v_min_f32_e32 v32, v32, v51
	v_max_f32_e32 v51, v55, v55
	v_and_or_b32 v34, v34, s4, 12
	v_and_or_b32 v36, v36, s4, 13
	v_add_f32_e32 v38, v19, v41
	v_add_f32_e32 v19, v19, v42
	v_max_f32_e32 v13, v11, v15
	v_min_f32_e32 v11, v11, v15
	v_max_f32_e32 v15, v5, v10
	v_and_or_b32 v21, v21, s4, 36
	v_and_or_b32 v25, v25, s4, 48
	v_add_f32_e32 v56, v27, v18
	v_add_f32_e32 v57, v27, v26
	v_max_f32_e32 v55, v54, v51
	v_min_f32_e32 v51, v54, v51
	v_and_or_b32 v38, v38, s4, 14
	v_and_or_b32 v19, v19, s4, 15
	v_min_f32_e32 v5, v5, v10
	v_max_f32_e32 v10, v15, v11
	v_min_f32_e32 v11, v15, v11
	v_max_f32_e32 v15, v36, v36
	v_and_or_b32 v56, v56, s4, 49
	v_and_or_b32 v57, v57, s4, 50
	v_max_f32_e32 v54, v53, v55
	v_min_f32_e32 v53, v53, v55
	v_max_f32_e32 v55, v32, v51
	v_max_f32_e32 v36, v34, v15
	v_min_f32_e32 v15, v34, v15
	v_max_f32_e32 v34, v38, v38
	v_min_f32_e32 v32, v32, v51
	v_max_f32_e32 v51, v55, v53
	v_min_f32_e32 v53, v55, v53
	v_max_f32_e32 v55, v21, v25
	v_min_f32_e32 v21, v21, v25
	v_max_f32_e32 v25, v57, v57
	v_max_f32_e32 v38, v34, v19
	v_min_f32_e32 v19, v34, v19
	v_max_f32_e32 v57, v56, v25
	v_min_f32_e32 v25, v56, v25
	v_max_f32_e32 v34, v36, v38
	v_min_f32_e32 v36, v36, v38
	v_max_f32_e32 v38, v15, v19
	v_max_f32_e32 v56, v55, v57
	v_min_f32_e32 v55, v55, v57
	v_max_f32_e32 v57, v21, v25
	v_min_f32_e32 v15, v15, v19
	v_max_f32_e32 v19, v38, v36
	v_min_f32_e32 v36, v38, v36
	v_min_f32_e32 v21, v21, v25
	v_max_f32_e32 v25, v57, v55
	v_min_f32_e32 v55, v57, v55
	v_max_f32_e32 v38, v13, v34
	v_min_f32_e32 v13, v13, v34
	v_max_f32_e32 v34, v11, v36
	v_max_f32_e32 v57, v54, v56
	v_min_f32_e32 v54, v54, v56
	v_max_f32_e32 v56, v53, v55
	v_min_f32_e32 v11, v11, v36
	v_max_f32_e32 v36, v34, v13
	v_min_f32_e32 v13, v34, v13
	v_max_f32_e32 v34, v10, v19
	v_min_f32_e32 v10, v10, v19
	v_max_f32_e32 v19, v5, v15
	v_min_f32_e32 v53, v53, v55
	v_max_f32_e32 v55, v56, v54
	v_min_f32_e32 v54, v56, v54
	v_max_f32_e32 v56, v51, v25
	v_min_f32_e32 v25, v51, v25
	v_max_f32_e32 v51, v32, v21
	v_min_f32_e32 v5, v5, v15
	v_max_f32_e32 v15, v19, v10
	v_min_f32_e32 v21, v32, v21
	v_max_f32_e32 v32, v51, v25
	v_min_f32_e32 v10, v19, v10
	v_max_f32_e32 v19, v34, v36
	v_min_f32_e32 v34, v34, v36
	v_max_f32_e32 v36, v15, v13
	v_min_f32_e32 v13, v15, v13
	v_min_f32_e32 v25, v51, v25
	v_max_f32_e32 v51, v56, v55
	v_min_f32_e32 v55, v56, v55
	v_max_f32_e32 v56, v32, v54
	v_min_f32_e32 v32, v32, v54
	v_max_f32_e32 v15, v10, v11
	v_min_f32_e32 v10, v10, v11
	v_min_f32_e32 v11, v40, v38
	v_max_f32_e32 v41, v4, v13
	v_max_f32_e32 v54, v25, v53
	v_min_f32_e32 v25, v25, v53
	v_min_f32_e32 v53, v58, v57
	v_max_f32_e32 v59, v30, v32
	v_min_f32_e32 v4, v4, v13
	v_max_f32_e32 v13, v41, v11
	v_min_f32_e32 v11, v41, v11
	v_max_f32_e32 v41, v8, v34
	v_min_f32_e32 v8, v8, v34
	v_max_f32_e32 v34, v3, v10
	v_min_f32_e32 v30, v30, v32
	v_max_f32_e32 v32, v59, v53
	v_min_f32_e32 v53, v59, v53
	v_max_f32_e32 v59, v50, v55
	v_min_f32_e32 v50, v50, v55
	v_max_f32_e32 v55, v24, v25
	v_min_f32_e32 v3, v3, v10
	v_max_f32_e32 v10, v34, v8
	v_min_f32_e32 v8, v34, v8
	v_min_f32_e32 v24, v24, v25
	v_max_f32_e32 v25, v55, v50
	v_min_f32_e32 v50, v55, v50
	v_max_f32_e32 v34, v41, v13
	v_min_f32_e32 v13, v41, v13
	v_max_f32_e32 v41, v10, v11
	v_min_f32_e32 v10, v10, v11
	v_max_f32_e32 v11, v8, v4
	v_min_f32_e32 v4, v8, v4
	v_max_f32_e32 v8, v7, v19
	v_min_f32_e32 v7, v7, v19
	v_max_f32_e32 v19, v6, v15
	v_max_f32_e32 v55, v59, v32
	v_min_f32_e32 v32, v59, v32
	v_max_f32_e32 v59, v25, v53
	v_min_f32_e32 v25, v25, v53
	v_max_f32_e32 v53, v50, v30
	v_min_f32_e32 v30, v50, v30
	v_max_f32_e32 v50, v49, v51
	v_min_f32_e32 v49, v49, v51
	v_max_f32_e32 v51, v48, v54
	v_min_f32_e32 v6, v6, v15
	v_max_f32_e32 v15, v19, v7
	v_min_f32_e32 v7, v19, v7
	v_max_f32_e32 v19, v9, v36
	v_min_f32_e32 v9, v9, v36
	v_max_f32_e32 v36, v2, v5
	v_min_f32_e32 v48, v48, v54
	v_max_f32_e32 v54, v51, v49
	v_min_f32_e32 v49, v51, v49
	v_max_f32_e32 v51, v52, v56
	v_min_f32_e32 v52, v52, v56
	v_max_f32_e32 v56, v23, v21
	v_min_f32_e32 v2, v2, v5
	v_max_f32_e32 v5, v36, v9
	v_min_f32_e32 v9, v36, v9
	v_max_f32_e32 v36, v19, v15
	v_min_f32_e32 v21, v23, v21
	v_max_f32_e32 v23, v56, v52
	v_min_f32_e32 v52, v56, v52
	v_and_b32_e32 v20, 0xffffff80, v72
	v_min_f32_e32 v15, v19, v15
	v_max_f32_e32 v19, v5, v7
	v_min_f32_e32 v5, v5, v7
	v_max_f32_e32 v7, v9, v6
	v_min_f32_e32 v6, v9, v6
	v_min_f32_e32 v9, v8, v34
	v_min_f32_e32 v42, v36, v13
	v_max_f32_e32 v56, v51, v54
	v_min_f32_e32 v51, v51, v54
	v_max_f32_e32 v54, v23, v49
	v_min_f32_e32 v23, v23, v49
	v_max_f32_e32 v49, v52, v48
	v_min_f32_e32 v48, v52, v48
	v_and_b32_e32 v39, 0xffffff80, v65
	v_min_f32_e32 v65, v48, v24
	v_max3_f32 v9, v9, v48, v24
	v_max3_f32 v24, v42, v49, v30
	v_add_f32_e32 v27, v27, v28
	v_add_f32_e32 v28, v20, v17
	v_add_f32_e32 v42, v20, v18
	v_add_f32_e32 v20, v20, v26
	v_and_b32_e32 v22, 0xffffff80, v73
	v_and_or_b32 v27, v27, s4, 51
	v_and_or_b32 v28, v28, s4, 64
	v_and_b32_e32 v42, 0xffffff00, v42
	v_and_b32_e32 v20, 0xffffff00, v20
	v_and_b32_e32 v29, 0xffffff80, v74
	v_and_b32_e32 v31, 0xffffff80, v75
	v_and_b32_e32 v33, 0xffffff80, v70
	v_and_b32_e32 v35, 0xffffff80, v71
	v_and_b32_e32 v37, 0xffffff80, v64
;     __device__ __forceinline__ void fused(f32x4 (&acc)[2][2][4][2], const Unit& u, int wr, int wc, int fr, int fq, PG8_LAS unsigned char* lds, int wid, int lane) const {
;     ...
;             { float cv[16]; cv[0] = __uint_as_float((__float_as_uint(v0[1] + v1[0]) & ~255u) | 16u); cv[1] = __uint_as_float((__float_as_uint(v0[1] + v1[1]) & ~255u) | 17u); cv[2] = __uint_as_float((__float_as_uint(v0[1] + v1[2]) & ~255u) | 18u); cv[3] = __uint_as_float((__float_as_uint(v0[1] + v1[3]) & ~255u) | 19u); cv[4] = __uint_as_float((__float_as_uint(v0[1] + v1[4]) & ~255u) | 20u); cv[5] = __uint_as_float((__float_as_uint(v0[1] + v1[5]) & ~255u) | 21u); cv[6] = __uint_as_float((__float_as_uint(v0[1] + v1[6]) & ~255u) | 22u); cv[7] = __uint_as_float((__float_as_uint(v0[1] + v1[7]) & ~255u) | 23u); cv[8] = __uint_as_float((__float_as_uint(v0[2] + v1[0]) & ~255u) | 32u); cv[9] = __uint_as_float((__float_as_uint(v0[2] + v1[1]) & ~255u) | 33u); cv[10] = __uint_as_float((__float_as_uint(v0[2] + v1[2]) & ~255u) | 34u); cv[11] = __uint_as_float((__float_as_uint(v0[2] + v1[3]) & ~255u) | 35u); cv[12] = __uint_as_float((__float_as_uint(v0[2] + v1[4]) & ~255u) | 36u); cv[13] = __uint_as_float((__float_as_uint(v0[3] + v1[0]) & ~255u) | 48u); cv[14] = __uint_as_float((__float_as_uint(v0[3] + v1[1]) & ~255u) | 49u); cv[15] = __uint_as_float((__float_as_uint(v0[3] + v1[2]) & ~255u) | 50u); sort16_desc(cv); merge_top16(best, cv); }
	v_min_f32_e32 v43, v15, v41
	v_min_f32_e32 v44, v19, v10
	v_min_f32_e32 v62, v54, v25
	v_or_b32_e32 v42, 0x41, v42
	v_or_b32_e32 v20, 0x42, v20
	v_add_f32_e32 v26, v22, v17
	v_add_f32_e32 v22, v22, v18
	v_min_f32_e32 v63, v23, v53
	v_max3_f32 v23, v43, v23, v53
	v_max3_f32 v10, v19, v10, v62
	v_max3_f32 v19, v44, v54, v25
	v_and_b32_e32 v26, 0xffffff00, v26
	v_and_b32_e32 v22, 0xffffff00, v22
	v_add_f32_e32 v43, v29, v17
	v_add_f32_e32 v29, v29, v18
	v_add_f32_e32 v44, v31, v17
	v_add_f32_e32 v18, v31, v18
	v_add_f32_e32 v31, v33, v17
	v_add_f32_e32 v33, v35, v17
	v_add_f32_e32 v35, v37, v17
	v_add_f32_e32 v37, v39, v17
	v_max_f32_e32 v39, v27, v28
	v_min_f32_e32 v27, v27, v28
	v_max_f32_e32 v28, v42, v42
	v_or_b32_e32 v26, 0x50, v26
	v_or_b32_e32 v22, 0x51, v22
	v_and_b32_e32 v43, 0xffffff00, v43
	v_and_b32_e32 v29, 0xffffff00, v29
	v_max_f32_e32 v42, v28, v20
	v_min_f32_e32 v20, v28, v20
	v_or_b32_e32 v43, 0x60, v43
	v_or_b32_e32 v29, 0x61, v29
	v_max_f32_e32 v28, v39, v42
	v_min_f32_e32 v39, v39, v42
	v_max_f32_e32 v42, v27, v20
	v_min_f32_e32 v20, v27, v20
	v_max_f32_e32 v27, v42, v39
	v_min_f32_e32 v39, v42, v39
	v_max_f32_e32 v42, v26, v22
	v_min_f32_e32 v22, v26, v22
	v_max_f32_e32 v26, v29, v29
	v_max_f32_e32 v29, v43, v43
	v_max_f32_e32 v43, v29, v26
	v_min_f32_e32 v26, v29, v26
	v_max_f32_e32 v29, v42, v43
	v_min_f32_e32 v42, v42, v43
	v_max_f32_e32 v43, v22, v26
	v_and_b32_e32 v12, 0xffffff80, v68
	v_and_b32_e32 v14, 0xffffff80, v69
	v_min_f32_e32 v22, v22, v26
	v_max_f32_e32 v26, v43, v42
	v_min_f32_e32 v42, v43, v42
	v_add_f32_e32 v12, v12, v17
	v_add_f32_e32 v14, v14, v17
	v_max_f32_e32 v43, v28, v29
	v_min_f32_e32 v28, v28, v29
	v_max_f32_e32 v29, v39, v42
	v_and_b32_e32 v44, 0xffffff00, v44
	v_and_b32_e32 v18, 0xffffff00, v18
	v_and_b32_e32 v12, 0xffffff00, v12
	v_and_b32_e32 v14, 0xffffff00, v14
	v_min_f32_e32 v39, v39, v42
	v_max_f32_e32 v42, v29, v28
	v_min_f32_e32 v28, v29, v28
	v_max_f32_e32 v29, v27, v26
	v_min_f32_e32 v26, v27, v26
	v_max_f32_e32 v27, v20, v22
	v_or_b32_e32 v44, 0x70, v44
	v_or_b32_e32 v18, 0x71, v18
	v_or_b32_e32 v12, 0x80, v12
	v_or_b32_e32 v14, 0x90, v14
	v_min_f32_e32 v20, v20, v22
	v_max_f32_e32 v22, v27, v26
	v_min_f32_e32 v26, v27, v26
	v_and_b32_e32 v31, 0xffffff00, v31
	v_and_b32_e32 v33, 0xffffff00, v33
	v_max_f32_e32 v27, v29, v42
	v_min_f32_e32 v29, v29, v42
	v_max_f32_e32 v42, v22, v28
	v_min_f32_e32 v22, v22, v28
	v_max_f32_e32 v28, v26, v39
	v_min_f32_e32 v26, v26, v39
	v_max_f32_e32 v39, v44, v44
	v_or_b32_e32 v31, 0xa0, v31
	v_or_b32_e32 v33, 0xb0, v33
	v_and_b32_e32 v35, 0xffffff00, v35
	v_and_b32_e32 v37, 0xffffff00, v37
	v_max_f32_e32 v44, v39, v18
	v_min_f32_e32 v18, v39, v18
	v_max_f32_e32 v39, v12, v14
	v_min_f32_e32 v12, v12, v14
	v_or_b32_e32 v35, 0xc0, v35
	v_or_b32_e32 v37, 0xd0, v37
	v_max_f32_e32 v14, v44, v39
	v_min_f32_e32 v39, v44, v39
	v_max_f32_e32 v44, v18, v12
	v_min_f32_e32 v12, v18, v12
	v_max_f32_e32 v18, v44, v39
	v_min_f32_e32 v39, v44, v39
	v_max_f32_e32 v44, v31, v33
	v_min_f32_e32 v31, v31, v33
	v_max_f32_e32 v33, v37, v37
	v_max_f32_e32 v37, v35, v33
	v_min_f32_e32 v33, v35, v33
	v_max_f32_e32 v35, v44, v37
	v_min_f32_e32 v37, v44, v37
	v_max_f32_e32 v44, v31, v33
	v_min_f32_e32 v31, v31, v33
	v_max_f32_e32 v33, v44, v37
	v_min_f32_e32 v37, v44, v37
	v_max_f32_e32 v44, v14, v35
	v_min_f32_e32 v14, v14, v35
	v_max_f32_e32 v35, v39, v37
	v_min_f32_e32 v37, v39, v37
	v_max_f32_e32 v39, v35, v14
	v_min_f32_e32 v14, v35, v14
	v_max_f32_e32 v35, v18, v33
	v_min_f32_e32 v18, v18, v33
	v_max_f32_e32 v33, v12, v31
	v_min_f32_e32 v12, v12, v31
	v_max_f32_e32 v31, v33, v18
	v_min_f32_e32 v45, v5, v11
	v_min_f32_e32 v61, v51, v59
	v_min_f32_e32 v18, v33, v18
	v_max_f32_e32 v33, v35, v39
	v_min_f32_e32 v35, v35, v39
	v_max_f32_e32 v39, v31, v14
	v_min_f32_e32 v14, v31, v14
	v_max3_f32 v5, v5, v11, v61
	v_max3_f32 v11, v45, v51, v59
	v_max_f32_e32 v31, v18, v37
	v_min_f32_e32 v18, v18, v37
	v_min_f32_e32 v37, v43, v44
	v_max_f32_e32 v45, v22, v14
	v_min_f32_e32 v14, v22, v14
	v_max_f32_e32 v22, v45, v37
	v_min_f32_e32 v37, v45, v37
	v_max_f32_e32 v45, v29, v35
	v_min_f32_e32 v29, v29, v35
	v_max_f32_e32 v35, v26, v18
	v_min_f32_e32 v46, v7, v4
	v_min_f32_e32 v47, v6, v3
	v_min_f32_e32 v52, v50, v55
	v_min_f32_e32 v60, v56, v32
	v_min_f32_e32 v64, v49, v30
	v_min_f32_e32 v18, v26, v18
	v_max_f32_e32 v26, v35, v29
	v_min_f32_e32 v29, v35, v29
	v_max3_f32 v21, v40, v38, v21
	v_max3_f32 v8, v8, v34, v65
	v_max3_f32 v13, v36, v13, v64
	v_max3_f32 v15, v15, v41, v63
	v_max3_f32 v4, v7, v4, v60
	v_max3_f32 v7, v46, v56, v32
	v_max3_f32 v3, v6, v3, v52
	v_max3_f32 v6, v47, v50, v55
	v_max3_f32 v2, v2, v58, v57
	v_max_f32_e32 v35, v45, v22
	v_min_f32_e32 v22, v45, v22
	v_max_f32_e32 v45, v26, v37
	v_min_f32_e32 v26, v26, v37
	v_max_f32_e32 v37, v29, v14
	v_min_f32_e32 v14, v29, v14
	v_max_f32_e32 v29, v27, v33
	v_min_f32_e32 v27, v27, v33
	v_max_f32_e32 v33, v28, v31
	v_max_f32_e32 v25, v21, v19
	v_min_f32_e32 v19, v21, v19
	v_max_f32_e32 v21, v8, v5
	v_min_f32_e32 v5, v8, v5
	v_max_f32_e32 v8, v9, v11
	v_min_f32_e32 v9, v9, v11
	v_max_f32_e32 v11, v13, v4
	v_min_f32_e32 v4, v13, v4
	v_max_f32_e32 v13, v24, v7
	v_min_f32_e32 v7, v24, v7
	v_max_f32_e32 v24, v15, v3
	v_min_f32_e32 v3, v15, v3
	v_max_f32_e32 v15, v23, v6
	v_min_f32_e32 v6, v23, v6
	v_max_f32_e32 v23, v10, v2
	v_min_f32_e32 v2, v10, v2
	v_min_f32_e32 v28, v28, v31
	v_max_f32_e32 v31, v33, v27
	v_min_f32_e32 v27, v33, v27
	v_max_f32_e32 v33, v42, v39
	v_min_f32_e32 v39, v42, v39
	v_max_f32_e32 v42, v20, v12
	v_max_f32_e32 v10, v25, v13
	v_min_f32_e32 v13, v25, v13
	v_max_f32_e32 v25, v21, v24
	v_min_f32_e32 v21, v21, v24
; __device__ __forceinline__ void merge_top16(float (&v)[16], const float (&nw)[16]) {
;     v[0] = fmaxf(v[0], nw[15]); v[1] = fmaxf(v[1], nw[14]); v[2] = fmaxf(v[2], nw[13]); v[3] = fmaxf(v[3], nw[12]); v[4] = fmaxf(v[4], nw[11]); v[5] = fmaxf(v[5], nw[10]); v[6] = fmaxf(v[6], nw[9]); v[7] = fmaxf(v[7], nw[8]); v[8] = fmaxf(v[8], nw[7]); v[9] = fmaxf(v[9], nw[6]); v[10] = fmaxf(v[10], nw[5]); v[11] = fmaxf(v[11], nw[4]); v[12] = fmaxf(v[12], nw[3]); v[13] = fmaxf(v[13], nw[2]); v[14] = fmaxf(v[14], nw[1]); v[15] = fmaxf(v[15], nw[0]);
;     CE(v[0], v[8]); CE(v[1], v[9]); CE(v[2], v[10]); CE(v[3], v[11]);
;     CE(v[4], v[12]); CE(v[5], v[13]); CE(v[6], v[14]); CE(v[7], v[15]);
;     CE(v[0], v[4]); CE(v[1], v[5]); CE(v[2], v[6]); CE(v[3], v[7]);
;     CE(v[8], v[12]); CE(v[9], v[13]); CE(v[10], v[14]); CE(v[11], v[15]);
;     CE(v[0], v[2]); CE(v[1], v[3]); CE(v[4], v[6]); CE(v[5], v[7]);
;     CE(v[8], v[10]); CE(v[9], v[11]); CE(v[12], v[14]); CE(v[13], v[15]);
;     __device__ __forceinline__ void fused(f32x4 (&acc)[2][2][4][2], const Unit& u, int wr, int wc, int fr, int fq, PG8_LAS unsigned char* lds, int wid, int lane) const {
;     ...
;             { float cv[16]; cv[0] = __uint_as_float((__float_as_uint(v0[14] + v1[0]) & ~255u) | 224u); cv[1] = __uint_as_float((__float_as_uint(v0[15] + v1[0]) & ~255u) | 240u); cv[2] = -INFINITY; cv[3] = -INFINITY; cv[4] = -INFINITY; cv[5] = -INFINITY; cv[6] = -INFINITY; cv[7] = -INFINITY; cv[8] = -INFINITY; cv[9] = -INFINITY; cv[10] = -INFINITY; cv[11] = -INFINITY; cv[12] = -INFINITY; cv[13] = -INFINITY; cv[14] = -INFINITY; cv[15] = -INFINITY; sort16_desc(cv); merge_top16(best, cv); }
;             float sc[16], sum = 0.f;
; #pragma unroll
;             for (int q = 0; q < 16; ++q) { sc[q] = __uint_as_float(__float_as_uint(best[q]) & ~255u); }
;             const float smax = sc[0];
; #pragma unroll
;             for (int q = 0; q < 16; ++q) { sc[q] = __builtin_amdgcn_exp2f((sc[q] - smax) * 1.4426950408889634f); }
; #pragma unroll
;             for (int q = 0; q < 16; ++q) sum += sc[q];
;             const float rs = 1.0f / sum;
;             asm volatile("s_waitcnt lgkmcnt(0)" ::: "memory");
;             int ex[16];
; #pragma unroll
;             for (int q = 0; q < 16; ++q) { const unsigned cid = __float_as_uint(best[q]) & 255u; ex[q] = idxl[cid >> 4] * 128 + idxl[16 + (cid & 15u)]; }
	v_max_f32_e32 v24, v8, v15
	v_min_f32_e32 v8, v8, v15
	v_max_f32_e32 v15, v11, v23
	v_min_f32_e32 v11, v11, v23
	v_max_f32_e32 v23, v19, v7
	v_min_f32_e32 v7, v19, v7
	v_max_f32_e32 v19, v5, v3
	v_min_f32_e32 v3, v5, v3
	v_max_f32_e32 v5, v9, v6
	v_min_f32_e32 v6, v9, v6
	v_max_f32_e32 v9, v4, v2
	v_min_f32_e32 v2, v4, v2
	v_min_f32_e32 v12, v20, v12
	v_max_f32_e32 v20, v42, v39
	v_min_f32_e32 v39, v42, v39
	v_and_b32_e32 v1, 0xffffff80, v66
	v_and_b32_e32 v0, 0xffffff80, v67
	v_max_f32_e32 v4, v10, v24
	v_min_f32_e32 v10, v10, v24
	v_max_f32_e32 v24, v25, v15
	v_min_f32_e32 v15, v25, v15
	v_max_f32_e32 v25, v13, v8
	v_min_f32_e32 v8, v13, v8
	v_max_f32_e32 v13, v21, v11
	v_min_f32_e32 v11, v21, v11
	v_max_f32_e32 v21, v23, v5
	v_min_f32_e32 v5, v23, v5
	v_max_f32_e32 v23, v19, v9
	v_min_f32_e32 v9, v19, v9
	v_max_f32_e32 v19, v7, v6
	v_min_f32_e32 v6, v7, v6
	v_max_f32_e32 v7, v3, v2
	v_min_f32_e32 v2, v3, v2
	v_max_f32_e32 v42, v33, v31
	v_min_f32_e32 v31, v33, v31
	v_max_f32_e32 v33, v20, v27
	v_min_f32_e32 v20, v20, v27
	v_max_f32_e32 v27, v39, v28
	v_min_f32_e32 v28, v39, v28
	v_min_f32_e32 v3, v4, v24
	v_min_f32_e32 v30, v10, v15
	v_min_f32_e32 v32, v25, v13
	v_min_f32_e32 v34, v8, v11
	v_min_f32_e32 v36, v21, v23
	v_min_f32_e32 v38, v5, v9
	v_min_f32_e32 v40, v19, v7
	v_min_f32_e32 v41, v6, v2
	v_max_f32_e32 v39, v29, v35
	v_min_f32_e32 v29, v29, v35
	v_max_f32_e32 v35, v42, v22
	v_min_f32_e32 v22, v42, v22
	v_max_f32_e32 v42, v31, v45
	v_min_f32_e32 v31, v31, v45
	v_max_f32_e32 v45, v33, v26
	v_min_f32_e32 v26, v33, v26
	v_max_f32_e32 v33, v20, v37
	v_min_f32_e32 v20, v20, v37
	v_max_f32_e32 v37, v27, v14
	v_min_f32_e32 v14, v27, v14
	v_max_f32_e32 v27, v28, v18
	v_min_f32_e32 v18, v28, v18
	v_add_f32_e32 v1, v1, v17
	v_add_f32_e32 v0, v0, v17
	v_max3_f32 v4, v4, v24, v12
	v_max_f32_e32 v3, v3, v18
	v_max3_f32 v10, v10, v15, v27
	v_max_f32_e32 v12, v30, v14
	v_max3_f32 v13, v25, v13, v37
	v_max_f32_e32 v14, v32, v20
	v_max3_f32 v8, v8, v11, v33
	v_max_f32_e32 v11, v34, v26
	v_max3_f32 v15, v21, v23, v45
	v_max_f32_e32 v18, v36, v31
	v_max3_f32 v5, v5, v9, v42
	v_max_f32_e32 v9, v38, v22
	v_max3_f32 v7, v19, v7, v35
	v_max_f32_e32 v19, v40, v29
	v_max3_f32 v2, v6, v2, v39
	v_max3_f32 v6, v41, v43, v44
	v_and_b32_e32 v1, 0xffffff00, v1
	v_and_b32_e32 v0, 0xffffff00, v0
	v_max_f32_e32 v20, v4, v15
	v_min_f32_e32 v4, v4, v15
	v_max_f32_e32 v15, v3, v18
	v_min_f32_e32 v3, v3, v18
	v_max_f32_e32 v18, v10, v5
	v_min_f32_e32 v5, v10, v5
	v_max_f32_e32 v10, v12, v9
	v_min_f32_e32 v9, v12, v9
	v_max_f32_e32 v12, v13, v7
	v_min_f32_e32 v7, v13, v7
	v_max_f32_e32 v13, v14, v19
	v_min_f32_e32 v14, v14, v19
	v_max_f32_e32 v19, v8, v2
	v_min_f32_e32 v2, v8, v2
	v_max_f32_e32 v8, v11, v6
	v_min_f32_e32 v6, v11, v6
	v_or_b32_e32 v1, 0xe0, v1
	v_or_b32_e32 v0, 0xf0, v0
	v_max_f32_e32 v11, v20, v12
	v_min_f32_e32 v12, v20, v12
	v_max_f32_e32 v20, v15, v13
	v_min_f32_e32 v13, v15, v13
	v_max_f32_e32 v15, v18, v19
	v_min_f32_e32 v18, v18, v19
	v_max_f32_e32 v19, v10, v8
	v_min_f32_e32 v8, v10, v8
	v_max_f32_e32 v10, v4, v7
	v_min_f32_e32 v4, v4, v7
	v_max_f32_e32 v7, v3, v14
	v_min_f32_e32 v3, v3, v14
	v_max_f32_e32 v14, v5, v2
	v_min_f32_e32 v2, v5, v2
	v_max_f32_e32 v5, v9, v6
	v_min_f32_e32 v6, v9, v6
	v_max_f32_e32 v9, v11, v15
	v_min_f32_e32 v11, v11, v15
	v_max_f32_e32 v15, v20, v19
	v_min_f32_e32 v19, v20, v19
	v_max_f32_e32 v20, v12, v18
	v_min_f32_e32 v12, v12, v18
	v_max_f32_e32 v18, v13, v8
	v_min_f32_e32 v8, v13, v8
	v_max_f32_e32 v13, v10, v14
	v_min_f32_e32 v10, v10, v14
	v_max_f32_e32 v14, v7, v5
	v_min_f32_e32 v5, v7, v5
	v_max_f32_e32 v7, v4, v2
	v_min_f32_e32 v2, v4, v2
	v_max_f32_e32 v4, v3, v6
	v_min_f32_e32 v3, v3, v6
	v_max_f32_e32 v17, v1, v0
	v_min_f32_e32 v0, v1, v0
	v_min_f32_e32 v6, v9, v15
	v_min_f32_e32 v21, v11, v19
	v_min_f32_e32 v22, v20, v18
	v_min_f32_e32 v23, v12, v8
	v_min_f32_e32 v24, v13, v14
	v_min_f32_e32 v25, v10, v5
	v_min_f32_e32 v26, v7, v4
	v_min_f32_e32 v27, v2, v3
	s_mov_b32 s4, 0xff800000
	v_max_f32_e32 v0, 0xff800000, v0
	v_max3_f32 v1, v9, v15, s4
	v_max_f32_e32 v6, 0xff800000, v6
	v_max3_f32 v9, v11, v19, s4
	v_max_f32_e32 v11, 0xff800000, v21
	v_max3_f32 v15, v20, v18, s4
	v_max_f32_e32 v18, 0xff800000, v22
	v_max3_f32 v8, v12, v8, s4
	v_max_f32_e32 v12, 0xff800000, v23
	v_max3_f32 v13, v13, v14, s4
	v_max_f32_e32 v14, 0xff800000, v24
	v_max3_f32 v5, v10, v5, s4
	v_max_f32_e32 v10, 0xff800000, v25
	v_max3_f32 v4, v7, v4, s4
	v_max_f32_e32 v7, 0xff800000, v26
	v_max3_f32 v0, v2, v3, v0
	v_max3_f32 v2, v27, v17, s4
	v_max_f32_e32 v3, v1, v13
	v_min_f32_e32 v1, v1, v13
	v_max_f32_e32 v13, v6, v14
	v_min_f32_e32 v6, v6, v14
	v_max_f32_e32 v14, v9, v5
	v_min_f32_e32 v5, v9, v5
	v_max_f32_e32 v9, v11, v10
	v_min_f32_e32 v10, v11, v10
	v_max_f32_e32 v11, v15, v4
	v_min_f32_e32 v4, v15, v4
	v_max_f32_e32 v15, v18, v7
	v_max_f32_e32 v17, v8, v0
	v_min_f32_e32 v0, v8, v0
	v_max_f32_e32 v8, v12, v2
	v_min_f32_e32 v2, v12, v2
	v_max_f32_e32 v12, v3, v11
	v_min_f32_e32 v3, v3, v11
	v_max_f32_e32 v11, v13, v15
	v_min_f32_e32 v13, v13, v15
	v_max_f32_e32 v15, v14, v17
	v_min_f32_e32 v14, v14, v17
	v_max_f32_e32 v17, v9, v8
	v_min_f32_e32 v8, v9, v8
	v_max_f32_e32 v9, v1, v4
	v_min_f32_e32 v24, v1, v4
	v_max_f32_e32 v27, v5, v0
	v_min_f32_e32 v28, v5, v0
	v_max_f32_e32 v29, v10, v2
	v_min_f32_e32 v30, v10, v2
	v_max_f32_e32 v0, v12, v15
	v_min_f32_e32 v1, v12, v15
	v_max_f32_e32 v2, v11, v17
	v_min_f32_e32 v4, v11, v17
	v_min_f32_e32 v7, v18, v7
	v_max_f32_e32 v33, v0, v2
	v_min_f32_e32 v34, v0, v2
	v_min_f32_e32 v36, v1, v4
	v_max_f32_e32 v25, v6, v7
	v_min_f32_e32 v26, v6, v7
	v_max_f32_e32 v35, v1, v4
	v_lshrrev_b32_e32 v0, 2, v33
	v_lshrrev_b32_e32 v2, 2, v34
	v_lshrrev_b32_e32 v6, 2, v36
	v_max_f32_e32 v17, v3, v14
	v_min_f32_e32 v31, v3, v14
	v_and_b32_e32 v0, 60, v0
	v_and_b32_e32 v1, 15, v33
	v_and_b32_e32 v2, 60, v2
	v_and_b32_e32 v3, 15, v34
	v_lshrrev_b32_e32 v4, 2, v35
	v_and_b32_e32 v5, 15, v35
	v_and_b32_e32 v6, 60, v6
	v_and_b32_e32 v7, 15, v36
	s_waitcnt lgkmcnt(0)
; #define RT_PK(q_) (ex[q_] | (int)((__float_as_uint(usc[ex[q_]]) >> 23) << 14))
;     __device__ __forceinline__ void fused(f32x4 (&acc)[2][2][4][2], const Unit& u, int wr, int wc, int fr, int fq, PG8_LAS unsigned char* lds, int wid, int lane) const {
;     ...
;             float sc[16], sum = 0.f;
; #pragma unroll
;             for (int q = 0; q < 16; ++q) { sc[q] = __uint_as_float(__float_as_uint(best[q]) & ~255u); }
;             const float smax = sc[0];
; #pragma unroll
;             for (int q = 0; q < 16; ++q) { sc[q] = __builtin_amdgcn_exp2f((sc[q] - smax) * 1.4426950408889634f); }
; #pragma unroll
;             for (int q = 0; q < 16; ++q) sum += sc[q];
;             const float rs = 1.0f / sum;
;             asm volatile("s_waitcnt lgkmcnt(0)" ::: "memory");
;             int ex[16];
; #pragma unroll
;             for (int q = 0; q < 16; ++q) { const unsigned cid = __float_as_uint(best[q]) & 255u; ex[q] = idxl[cid >> 4] * 128 + idxl[16 + (cid & 15u)]; }
;             const size_t o = ((size_t)u.pn * 16384 + (size_t)(u.pm * BM + row)) * 16;
;             typedef int i32x4 __attribute__((ext_vector_type(4)));
; #pragma unroll
;             for (int i = 0; i < 4; ++i) {
;     ...
;                 *(i32x4*)(eidx + o + 4 * i) = (i32x4){RT_PK(4 * i), RT_PK(4 * i + 1), RT_PK(4 * i + 2), RT_PK(4 * i + 3)};
;                 *(f32x4*)(egate + o + 4 * i) = (f32x4){sc[4 * i] * rs * vsc[ex[4 * i]], sc[4 * i + 1] * rs * vsc[ex[4 * i + 1]], sc[4 * i + 2] * rs * vsc[ex[4 * i + 2]], sc[4 * i + 3] * rs * vsc[ex[4 * i + 3]]};
	v_add_u32_e32 v0, v16, v0
	v_lshl_add_u32 v1, v1, 2, v16
	v_add_u32_e32 v2, v16, v2
	v_lshl_add_u32 v3, v3, 2, v16
	v_and_b32_e32 v4, 60, v4
	v_lshl_add_u32 v5, v5, 2, v16
	v_add_u32_e32 v6, v16, v6
	v_lshl_add_u32 v7, v7, 2, v16
	v_add_u32_e32 v4, v16, v4
	ds_read_b32 v0, v0
	ds_read_b32 v1, v1 offset:64
	ds_read_b32 v2, v2
	ds_read_b32 v3, v3 offset:64
	ds_read_b32 v10, v4
	ds_read_b32 v5, v5 offset:64
	ds_read_b32 v6, v6
	ds_read_b32 v7, v7 offset:64
	s_waitcnt lgkmcnt(0)
	v_lshl_add_u32 v0, v0, 7, v1
	v_ashrrev_i32_e32 v1, 31, v0
	v_lshl_add_u32 v4, v2, 7, v3
	v_lshlrev_b64 v[14:15], 3, v[0:1]
	v_lshl_add_u32 v10, v10, 7, v5
	v_lshl_add_u32 v12, v6, 7, v7
	v_lshl_add_u64 v[2:3], s[8:9], 0, v[14:15]
	v_ashrrev_i32_e32 v5, 31, v4
	v_max_f32_e32 v32, v13, v8
	v_min_f32_e32 v8, v13, v8
	global_load_dwordx2 v[170:171], v[2:3], off
	v_lshlrev_b64 v[18:19], 3, v[4:5]
	v_ashrrev_i32_e32 v11, 31, v10
	v_ashrrev_i32_e32 v13, 31, v12
	v_lshl_add_u64 v[2:3], s[8:9], 0, v[18:19]
	v_lshlrev_b64 v[20:21], 3, v[10:11]
	v_lshlrev_b64 v[22:23], 3, v[12:13]
	v_lshl_add_u64 v[6:7], s[8:9], 0, v[20:21]
	global_load_dwordx2 v[172:173], v[2:3], off
	global_load_dwordx2 v[174:175], v[6:7], off
	v_lshl_add_u64 v[2:3], s[8:9], 0, v[22:23]
	global_load_dwordx2 v[176:177], v[2:3], off
	v_min_f32_e32 v2, v9, v27
	v_min_f32_e32 v6, v25, v29
	v_max_f32_e32 v43, v2, v6
	v_min_f32_e32 v44, v2, v6
	v_and_b32_e32 v2, 0xffffff00, v34
	v_and_b32_e32 v51, 0xffffff00, v33
	v_max_f32_e32 v37, v9, v27
	v_max_f32_e32 v3, v25, v29
	v_sub_f32_e32 v2, v2, v51
	v_min_f32_e32 v9, v24, v28
	v_min_f32_e32 v25, v26, v30
	v_max_f32_e32 v41, v37, v3
	v_min_f32_e32 v42, v37, v3
	v_and_b32_e32 v3, 0xffffff00, v35
	v_mul_f32_e32 v2, 0x3fb8aa3b, v2
	v_max_f32_e32 v47, v9, v25
	v_min_f32_e32 v48, v9, v25
	v_exp_f32_e32 v25, v2
	v_sub_f32_e32 v2, v3, v51
	v_and_b32_e32 v6, 0xffffff00, v36
	v_mul_f32_e32 v2, 0x3fb8aa3b, v2
	v_max_f32_e32 v7, v24, v28
	v_max_f32_e32 v24, v26, v30
	v_max_f32_e32 v38, v17, v32
	v_exp_f32_e32 v26, v2
	v_sub_f32_e32 v2, v6, v51
	v_max_f32_e32 v45, v7, v24
	v_min_f32_e32 v46, v7, v24
	v_and_b32_e32 v7, 0xffffff00, v38
	v_mul_f32_e32 v2, 0x3fb8aa3b, v2
	v_min_f32_e32 v17, v17, v32
	v_exp_f32_e32 v27, v2
	v_sub_f32_e32 v2, v7, v51
	v_max_f32_e32 v39, v31, v8
	v_min_f32_e32 v40, v31, v8
	v_and_b32_e32 v8, 0xffffff00, v17
	v_mul_f32_e32 v2, 0x3fb8aa3b, v2
	v_exp_f32_e32 v28, v2
	v_sub_f32_e32 v2, v8, v51
	v_and_b32_e32 v9, 0xffffff00, v39
	v_mul_f32_e32 v2, 0x3fb8aa3b, v2
	v_exp_f32_e32 v29, v2
	v_sub_f32_e32 v2, v9, v51
	v_and_b32_e32 v31, 0xffffff00, v40
	v_mul_f32_e32 v2, 0x3fb8aa3b, v2
	v_exp_f32_e32 v30, v2
	v_sub_f32_e32 v2, v31, v51
	v_and_b32_e32 v32, 0xffffff00, v41
	v_mul_f32_e32 v2, 0x3fb8aa3b, v2
	v_exp_f32_e32 v31, v2
	v_sub_f32_e32 v2, v32, v51
	v_and_b32_e32 v34, 0xffffff00, v42
	v_mul_f32_e32 v2, 0x3fb8aa3b, v2
	v_exp_f32_e32 v6, v2
	v_sub_f32_e32 v2, v34, v51
	v_and_b32_e32 v35, 0xffffff00, v43
	v_mul_f32_e32 v2, 0x3fb8aa3b, v2
	v_exp_f32_e32 v7, v2
	v_sub_f32_e32 v2, v35, v51
	v_mul_f32_e32 v2, 0x3fb8aa3b, v2
	v_exp_f32_e32 v8, v2
	v_lshl_or_b32 v2, s18, 8, v128
	v_ashrrev_i32_e32 v3, 31, v2
	s_lshl_b64 s[4:5], s[16:17], 18
	v_lshl_add_u64 v[32:33], v[2:3], 4, s[4:5]
	s_mov_b32 s4, 0x7fc000
	v_sub_f32_e32 v24, v51, v51
	v_mul_f32_e32 v24, 0x3fb8aa3b, v24
	v_exp_f32_e32 v24, v24
	s_waitcnt vmcnt(0)
	v_lshrrev_b32_e32 v1, 9, v170
	v_and_or_b32 v2, v1, s4, v0
	v_and_b32_e32 v36, 0xffffff00, v44
	v_and_b32_e32 v37, 0xffffff00, v45
	v_and_b32_e32 v49, 0xffffff00, v46
	v_and_b32_e32 v50, 0xffffff00, v47
	v_and_b32_e32 v52, 0xffffff00, v48
	v_lshrrev_b32_e32 v0, 9, v172
	v_and_or_b32 v3, v0, s4, v4
	v_lshrrev_b32_e32 v0, 9, v174
	v_and_or_b32 v4, v0, s4, v10
	v_lshrrev_b32_e32 v0, 9, v176
	v_and_or_b32 v5, v0, s4, v12
	v_lshlrev_b64 v[12:13], 2, v[32:33]
	v_lshl_add_u64 v[0:1], s[12:13], 0, v[12:13]
	s_nop 0
	v_readfirstlane_b32 s98, v0
	v_readfirstlane_b32 s99, v1
	v_lshrrev_b32_e32 v202, 6, v128
	v_and_b32_e32 v203, 63, v128
	v_lshlrev_b32_e32 v202, 13, v202
	v_lshl_or_b32 v204, v203, 6, v202
	v_lshl_or_b32 v205, v203, 4, v202
	v_lshlrev_b32_e32 v203, 4, v203
	ds_write_b128 v204, v[2:5]
	v_lshrrev_b32_e32 v32, 2, v40
	v_add_f32_e32 v10, 0, v24
	v_add_f32_e32 v10, v25, v10
	v_add_f32_e32 v10, v26, v10
	v_add_f32_e32 v10, v27, v10
	v_sub_f32_e32 v2, v36, v51
	v_add_f32_e32 v10, v28, v10
	v_mul_f32_e32 v2, 0x3fb8aa3b, v2
	v_add_f32_e32 v10, v29, v10
	v_exp_f32_e32 v9, v2
	v_sub_f32_e32 v2, v37, v51
	v_add_f32_e32 v10, v30, v10
	v_mul_f32_e32 v2, 0x3fb8aa3b, v2
	v_sub_f32_e32 v3, v49, v51
	v_add_f32_e32 v10, v31, v10
	v_exp_f32_e32 v2, v2
	v_mul_f32_e32 v3, 0x3fb8aa3b, v3
	v_sub_f32_e32 v4, v50, v51
	v_add_f32_e32 v10, v6, v10
	v_exp_f32_e32 v3, v3
	v_mul_f32_e32 v4, 0x3fb8aa3b, v4
	v_sub_f32_e32 v5, v52, v51
	v_add_f32_e32 v10, v7, v10
	v_exp_f32_e32 v4, v4
	v_mul_f32_e32 v5, 0x3fb8aa3b, v5
	v_add_f32_e32 v10, v8, v10
	v_exp_f32_e32 v5, v5
	v_add_f32_e32 v10, v9, v10
	v_add_f32_e32 v10, v2, v10
	v_lshrrev_b32_e32 v11, 2, v38
	v_lshrrev_b32_e32 v15, 2, v17
	v_add_f32_e32 v10, v3, v10
	v_and_b32_e32 v11, 60, v11
	v_and_b32_e32 v14, 15, v38
	v_and_b32_e32 v15, 60, v15
	v_and_b32_e32 v17, 15, v17
	v_lshrrev_b32_e32 v22, 2, v39
	v_and_b32_e32 v23, 15, v39
	v_and_b32_e32 v33, 15, v40
	v_add_f32_e32 v10, v4, v10
	v_add_u32_e32 v11, v16, v11
	v_lshl_add_u32 v14, v14, 2, v16
	v_add_u32_e32 v15, v16, v15
	v_lshl_add_u32 v17, v17, 2, v16
	v_and_b32_e32 v22, 60, v22
	v_lshl_add_u32 v23, v23, 2, v16
	v_and_b32_e32 v32, 60, v32
	v_lshl_add_u32 v33, v33, 2, v16
	v_add_f32_e32 v10, v5, v10
	v_add_u32_e32 v22, v16, v22
	v_add_u32_e32 v32, v16, v32
	ds_read_b32 v11, v11
	ds_read_b32 v14, v14 offset:64
	ds_read_b32 v15, v15
	ds_read_b32 v17, v17 offset:64
	ds_read_b32 v34, v22
	ds_read_b32 v23, v23 offset:64
	ds_read_b32 v35, v32
	ds_read_b32 v33, v33 offset:64
	s_waitcnt lgkmcnt(6)
; #define RT_PK(q_) (ex[q_] | (int)((__float_as_uint(usc[ex[q_]]) >> 23) << 14))
;     __device__ __forceinline__ void fused(f32x4 (&acc)[2][2][4][2], const Unit& u, int wr, int wc, int fr, int fq, PG8_LAS unsigned char* lds, int wid, int lane) const {
;     ...
;             for (int q = 0; q < 16; ++q) { sc[q] = __builtin_amdgcn_exp2f((sc[q] - smax) * 1.4426950408889634f); }
; #pragma unroll
;             for (int q = 0; q < 16; ++q) sum += sc[q];
;             const float rs = 1.0f / sum;
;             asm volatile("s_waitcnt lgkmcnt(0)" ::: "memory");
;             int ex[16];
; #pragma unroll
;             for (int q = 0; q < 16; ++q) { const unsigned cid = __float_as_uint(best[q]) & 255u; ex[q] = idxl[cid >> 4] * 128 + idxl[16 + (cid & 15u)]; }
;             const size_t o = ((size_t)u.pn * 16384 + (size_t)(u.pm * BM + row)) * 16;
;             typedef int i32x4 __attribute__((ext_vector_type(4)));
; #pragma unroll
;             for (int i = 0; i < 4; ++i) {
;     ...
;                 *(i32x4*)(eidx + o + 4 * i) = (i32x4){RT_PK(4 * i), RT_PK(4 * i + 1), RT_PK(4 * i + 2), RT_PK(4 * i + 3)};
;                 *(f32x4*)(egate + o + 4 * i) = (f32x4){sc[4 * i] * rs * vsc[ex[4 * i]], sc[4 * i + 1] * rs * vsc[ex[4 * i + 1]], sc[4 * i + 2] * rs * vsc[ex[4 * i + 2]], sc[4 * i + 3] * rs * vsc[ex[4 * i + 3]]};
	v_lshl_add_u32 v14, v11, 7, v14
	v_div_scale_f32 v11, s[16:17], v10, v10, 1.0
	v_rcp_f32_e32 v36, v11
	s_waitcnt lgkmcnt(4)
	v_lshl_add_u32 v22, v15, 7, v17
	s_waitcnt lgkmcnt(2)
	v_lshl_add_u32 v32, v34, 7, v23
	s_waitcnt lgkmcnt(0)
	v_lshl_add_u32 v34, v35, 7, v33
	v_fma_f32 v15, -v11, v36, 1.0
	v_fmac_f32_e32 v36, v15, v36
	v_div_scale_f32 v15, vcc, 1.0, v10, 1.0
	v_mul_f32_e32 v17, v15, v36
	v_fma_f32 v23, -v11, v17, v15
	v_fmac_f32_e32 v17, v23, v36
	v_fma_f32 v11, -v11, v17, v15
	v_div_fmas_f32 v11, v11, v36, v17
	v_div_fixup_f32 v10, v11, v10, 1.0
	v_pk_mul_f32 v[24:25], v[24:25], v[10:11] op_sel_hi:[1,0]
	v_pk_mul_f32 v[26:27], v[26:27], v[10:11] op_sel_hi:[1,0]
	v_ashrrev_i32_e32 v15, 31, v14
	v_ashrrev_i32_e32 v33, 31, v32
	v_lshl_add_u64 v[12:13], s[10:11], 0, v[12:13]
	s_nop 0
	v_readfirstlane_b32 s100, v12
	v_readfirstlane_b32 s101, v13
	v_ashrrev_i32_e32 v23, 31, v22
	v_lshlrev_b64 v[36:37], 3, v[32:33]
	v_lshl_add_u64 v[38:39], s[8:9], 0, v[36:37]
	v_ashrrev_i32_e32 v35, 31, v34
	v_mul_f32_e32 v18, v24, v171
	v_mul_f32_e32 v19, v25, v173
	v_lshlrev_b64 v[24:25], 3, v[14:15]
	v_mul_f32_e32 v20, v26, v175
	v_mul_f32_e32 v21, v27, v177
	ds_write_b128 v204, v[18:21] offset:4096
	v_lshlrev_b64 v[26:27], 3, v[22:23]
	s_nop 0
	v_lshl_add_u64 v[18:19], s[8:9], 0, v[24:25]
	v_lshl_add_u64 v[20:21], s[8:9], 0, v[26:27]
	global_load_dwordx2 v[178:179], v[18:19], off
	global_load_dwordx2 v[180:181], v[20:21], off
	global_load_dwordx2 v[182:183], v[38:39], off
	v_lshlrev_b64 v[38:39], 3, v[34:35]
	v_lshl_add_u64 v[18:19], s[8:9], 0, v[38:39]
	global_load_dwordx2 v[184:185], v[18:19], off
	s_waitcnt vmcnt(3)
	v_lshrrev_b32_e32 v11, 9, v178
	v_and_or_b32 v18, v11, s4, v14
	s_waitcnt vmcnt(2)
	v_lshrrev_b32_e32 v11, 9, v180
	v_and_or_b32 v19, v11, s4, v22
	s_waitcnt vmcnt(1)
	v_lshrrev_b32_e32 v11, 9, v182
	v_and_or_b32 v20, v11, s4, v32
	s_waitcnt vmcnt(0)
	v_lshrrev_b32_e32 v11, 9, v184
	v_and_or_b32 v21, v11, s4, v34
	ds_write_b128 v204, v[18:21] offset:16
	v_lshrrev_b32_e32 v11, 2, v41
	v_lshrrev_b32_e32 v15, 2, v42
	v_lshrrev_b32_e32 v18, 2, v43
	v_lshrrev_b32_e32 v20, 2, v44
	v_and_b32_e32 v11, 60, v11
	v_and_b32_e32 v14, 15, v41
	v_and_b32_e32 v15, 60, v15
	v_and_b32_e32 v17, 15, v42
	v_and_b32_e32 v18, 60, v18
	v_and_b32_e32 v19, 15, v43
	v_and_b32_e32 v20, 60, v20
	v_and_b32_e32 v21, 15, v44
	v_add_u32_e32 v11, v16, v11
	v_lshl_add_u32 v14, v14, 2, v16
	v_add_u32_e32 v15, v16, v15
	v_lshl_add_u32 v17, v17, 2, v16
	v_add_u32_e32 v18, v16, v18
	v_lshl_add_u32 v19, v19, 2, v16
	v_add_u32_e32 v20, v16, v20
	v_lshl_add_u32 v21, v21, 2, v16
	ds_read_b32 v11, v11
	ds_read_b32 v14, v14 offset:64
	ds_read_b32 v15, v15
	ds_read_b32 v17, v17 offset:64
	ds_read_b32 v18, v18
	ds_read_b32 v19, v19 offset:64
	ds_read_b32 v20, v20
	ds_read_b32 v21, v21 offset:64
	s_waitcnt lgkmcnt(6)
	v_lshl_add_u32 v14, v11, 7, v14
	s_waitcnt lgkmcnt(4)
	v_lshl_add_u32 v22, v15, 7, v17
	s_waitcnt lgkmcnt(2)
	v_lshl_add_u32 v32, v18, 7, v19
	v_pk_mul_f32 v[18:19], v[28:29], v[10:11] op_sel_hi:[1,0]
	s_waitcnt lgkmcnt(0)
	v_lshl_add_u32 v34, v20, 7, v21
	v_pk_mul_f32 v[20:21], v[30:31], v[10:11] op_sel_hi:[1,0]
	v_ashrrev_i32_e32 v15, 31, v14
	v_ashrrev_i32_e32 v33, 31, v32
	v_ashrrev_i32_e32 v23, 31, v22
	v_lshlrev_b64 v[28:29], 3, v[32:33]
	v_lshl_add_u64 v[30:31], s[8:9], 0, v[28:29]
	v_ashrrev_i32_e32 v35, 31, v34
	v_mul_f32_e32 v20, v20, v183
	v_mul_f32_e32 v21, v21, v185
	v_mul_f32_e32 v18, v18, v179
	v_mul_f32_e32 v19, v19, v181
	v_lshlrev_b64 v[24:25], 3, v[14:15]
	ds_write_b128 v204, v[18:21] offset:4112
	v_lshlrev_b64 v[26:27], 3, v[22:23]
	s_nop 0
	v_lshl_add_u64 v[18:19], s[8:9], 0, v[24:25]
	v_lshl_add_u64 v[20:21], s[8:9], 0, v[26:27]
	global_load_dwordx2 v[186:187], v[18:19], off
	global_load_dwordx2 v[188:189], v[20:21], off
	global_load_dwordx2 v[190:191], v[30:31], off
	v_lshlrev_b64 v[30:31], 3, v[34:35]
	v_lshl_add_u64 v[18:19], s[8:9], 0, v[30:31]
	global_load_dwordx2 v[192:193], v[18:19], off
	s_waitcnt vmcnt(3)
; #define RT_PK(q_) (ex[q_] | (int)((__float_as_uint(usc[ex[q_]]) >> 23) << 14))
;     __device__ __forceinline__ void fused(f32x4 (&acc)[2][2][4][2], const Unit& u, int wr, int wc, int fr, int fq, PG8_LAS unsigned char* lds, int wid, int lane) const {
;     ...
;             for (int q = 0; q < 16; ++q) { const unsigned cid = __float_as_uint(best[q]) & 255u; ex[q] = idxl[cid >> 4] * 128 + idxl[16 + (cid & 15u)]; }
;             const size_t o = ((size_t)u.pn * 16384 + (size_t)(u.pm * BM + row)) * 16;
;             typedef int i32x4 __attribute__((ext_vector_type(4)));
; #pragma unroll
;             for (int i = 0; i < 4; ++i) {
;     ...
;                 *(i32x4*)(eidx + o + 4 * i) = (i32x4){RT_PK(4 * i), RT_PK(4 * i + 1), RT_PK(4 * i + 2), RT_PK(4 * i + 3)};
;                 *(f32x4*)(egate + o + 4 * i) = (f32x4){sc[4 * i] * rs * vsc[ex[4 * i]], sc[4 * i + 1] * rs * vsc[ex[4 * i + 1]], sc[4 * i + 2] * rs * vsc[ex[4 * i + 2]], sc[4 * i + 3] * rs * vsc[ex[4 * i + 3]]};
	v_lshrrev_b32_e32 v11, 9, v186
	v_and_or_b32 v18, v11, s4, v14
	s_waitcnt vmcnt(2)
	v_lshrrev_b32_e32 v11, 9, v188
	v_and_or_b32 v19, v11, s4, v22
	s_waitcnt vmcnt(1)
	v_lshrrev_b32_e32 v11, 9, v190
	v_and_or_b32 v20, v11, s4, v32
	s_waitcnt vmcnt(0)
	v_lshrrev_b32_e32 v11, 9, v192
	v_and_or_b32 v21, v11, s4, v34
	ds_write_b128 v204, v[18:21] offset:32
	v_lshrrev_b32_e32 v11, 2, v45
	v_lshrrev_b32_e32 v15, 2, v46
	v_lshrrev_b32_e32 v18, 2, v47
	v_lshrrev_b32_e32 v20, 2, v48
	v_and_b32_e32 v11, 60, v11
	v_and_b32_e32 v14, 15, v45
	v_and_b32_e32 v15, 60, v15
	v_and_b32_e32 v17, 15, v46
	v_and_b32_e32 v18, 60, v18
	v_and_b32_e32 v19, 15, v47
	v_and_b32_e32 v20, 60, v20
	v_add_u32_e32 v11, v16, v11
	v_lshl_add_u32 v14, v14, 2, v16
	v_add_u32_e32 v15, v16, v15
	v_lshl_add_u32 v17, v17, 2, v16
	v_add_u32_e32 v18, v16, v18
	v_lshl_add_u32 v19, v19, 2, v16
	v_add_u32_e32 v20, v16, v20
	v_and_b32_e32 v21, 15, v48
	v_lshl_add_u32 v16, v21, 2, v16
	ds_read_b32 v11, v11
	ds_read_b32 v14, v14 offset:64
	ds_read_b32 v15, v15
	ds_read_b32 v17, v17 offset:64
	ds_read_b32 v18, v18
	ds_read_b32 v19, v19 offset:64
	ds_read_b32 v20, v20
	ds_read_b32 v21, v16 offset:64
	s_waitcnt lgkmcnt(6)
	v_lshl_add_u32 v14, v11, 7, v14
	s_waitcnt lgkmcnt(4)
	v_lshl_add_u32 v16, v15, 7, v17
	s_waitcnt lgkmcnt(2)
	v_lshl_add_u32 v18, v18, 7, v19
	v_pk_mul_f32 v[6:7], v[6:7], v[10:11] op_sel_hi:[1,0]
	v_pk_mul_f32 v[8:9], v[8:9], v[10:11] op_sel_hi:[1,0]
	v_ashrrev_i32_e32 v15, 31, v14
	v_ashrrev_i32_e32 v19, 31, v18
	s_waitcnt lgkmcnt(0)
	v_lshl_add_u32 v20, v20, 7, v21
	v_lshlrev_b64 v[22:23], 3, v[14:15]
	v_ashrrev_i32_e32 v17, 31, v16
	v_ashrrev_i32_e32 v21, 31, v20
	v_mul_f32_e32 v8, v8, v191
	v_mul_f32_e32 v9, v9, v193
	v_mul_f32_e32 v6, v6, v187
	v_mul_f32_e32 v7, v7, v189
	v_lshlrev_b64 v[26:27], 3, v[18:19]
	ds_write_b128 v204, v[6:9] offset:4128
	v_lshlrev_b64 v[24:25], 3, v[16:17]
	v_lshl_add_u64 v[28:29], s[8:9], 0, v[26:27]
	v_lshl_add_u64 v[6:7], s[8:9], 0, v[22:23]
	v_lshl_add_u64 v[8:9], s[8:9], 0, v[24:25]
	global_load_dwordx2 v[194:195], v[6:7], off
	global_load_dwordx2 v[196:197], v[8:9], off
	global_load_dwordx2 v[198:199], v[28:29], off
	v_lshlrev_b64 v[28:29], 3, v[20:21]
	v_lshl_add_u64 v[6:7], s[8:9], 0, v[28:29]
	global_load_dwordx2 v[200:201], v[6:7], off
	s_waitcnt vmcnt(3)
	v_lshrrev_b32_e32 v6, 9, v194
	s_waitcnt vmcnt(2)
	v_lshrrev_b32_e32 v7, 9, v196
	s_waitcnt vmcnt(1)
	v_lshrrev_b32_e32 v8, 9, v198
	v_and_or_b32 v6, v6, s4, v14
	v_and_or_b32 v7, v7, s4, v16
	s_waitcnt vmcnt(0)
	v_lshrrev_b32_e32 v9, 9, v200
	v_and_or_b32 v8, v8, s4, v18
	v_and_or_b32 v9, v9, s4, v20
	ds_write_b128 v204, v[6:9] offset:48
	v_pk_mul_f32 v[0:1], v[2:3], v[10:11] op_sel_hi:[1,0]
	v_pk_mul_f32 v[2:3], v[4:5], v[10:11] op_sel_hi:[1,0]
	v_mul_f32_e32 v0, v0, v195
	v_mul_f32_e32 v1, v1, v197
	v_mul_f32_e32 v2, v2, v199
	v_mul_f32_e32 v3, v3, v201
	ds_write_b128 v204, v[0:3] offset:4144
	s_waitcnt lgkmcnt(0)
	ds_read_b128 v[140:143], v205
	ds_read_b128 v[144:147], v205 offset:1024
	ds_read_b128 v[148:151], v205 offset:2048
	ds_read_b128 v[152:155], v205 offset:3072
	ds_read_b128 v[156:159], v205 offset:4096
	ds_read_b128 v[160:163], v205 offset:5120
	ds_read_b128 v[164:167], v205 offset:6144
	ds_read_b128 v[206:209], v205 offset:7168
	s_waitcnt lgkmcnt(0)
	global_store_dwordx4 v203, v[140:143], s[98:99]
	global_store_dwordx4 v203, v[144:147], s[98:99] offset:1024
	global_store_dwordx4 v203, v[148:151], s[98:99] offset:2048
	global_store_dwordx4 v203, v[152:155], s[98:99] offset:3072
	global_store_dwordx4 v203, v[156:159], s[100:101]
	global_store_dwordx4 v203, v[160:163], s[100:101] offset:1024
	global_store_dwordx4 v203, v[164:167], s[100:101] offset:2048
	global_store_dwordx4 v203, v[206:209], s[100:101] offset:3072

; #define PG8_LAS __attribute__((address_space(3)))
;     __device__ __forceinline__ void fused(f32x4 (&acc)[2][2][4][2], const Unit& u, int wr, int wc, int fr, int fq, PG8_LAS unsigned char* lds, int wid, int lane) const {
;     ...
;         if (half == 0) {
;             PG8_LAS int* idxl = (PG8_LAS int*)(lds + 65536) + row * 32;
;             float v0[16], v1[16];
; #pragma unroll
;             for (int q = 0; q < 16; ++q) { const unsigned b0 = __float_as_uint(top0[q]), b1 = __float_as_uint(top1[q]);
;                 v0[q] = __uint_as_float(b0 & ~127u); v1[q] = __uint_as_float(b1 & ~127u); idxl[q] = (int)(b0 & 127u); idxl[16 + q] = (int)(b1 & 127u); }
;             float best[16];
;             { float cv[16]; cv[0] = __uint_as_float((__float_as_uint(v0[0] + v1[0]) & ~255u) | 0u); cv[1] = __uint_as_float((__float_as_uint(v0[0] + v1[1]) & ~255u) | 1u); cv[2] = __uint_as_float((__float_as_uint(v0[0] + v1[2]) & ~255u) | 2u); cv[3] = __uint_as_float((__float_as_uint(v0[0] + v1[3]) & ~255u) | 3u); cv[4] = __uint_as_float((__float_as_uint(v0[0] + v1[4]) & ~255u) | 4u); cv[5] = __uint_as_float((__float_as_uint(v0[0] + v1[5]) & ~255u) | 5u); cv[6] = __uint_as_float((__float_as_uint(v0[0] + v1[6]) & ~255u) | 6u); cv[7] = __uint_as_float((__float_as_uint(v0[0] + v1[7]) & ~255u) | 7u); cv[8] = __uint_as_float((__float_as_uint(v0[0] + v1[8]) & ~255u) | 8u); cv[9] = __uint_as_float((__float_as_uint(v0[0] + v1[9]) & ~255u) | 9u); cv[10] = __uint_as_float((__float_as_uint(v0[0] + v1[10]) & ~255u) | 10u); cv[11] = __uint_as_float((__float_as_uint(v0[0] + v1[11]) & ~255u) | 11u); cv[12] = __uint_as_float((__float_as_uint(v0[0] + v1[12]) & ~255u) | 12u); cv[13] = __uint_as_float((__float_as_uint(v0[0] + v1[13]) & ~255u) | 13u); cv[14] = __uint_as_float((__float_as_uint(v0[0] + v1[14]) & ~255u) | 14u); cv[15] = __uint_as_float((__float_as_uint(v0[0] + v1[15]) & ~255u) | 15u); sort16_desc(cv);
; #pragma unroll
;               for (int q = 0; q < 16; ++q) best[q] = cv[q]; }
.LBB0_606:
	s_waitcnt lgkmcnt(0)
	s_barrier
	s_and_b64 vcc, exec, s[4:5]
	s_cbranch_vccnz .LBB0_608
	v_lshl_add_u32 v16, v128, 7, 0
	v_add_u32_e32 v16, 0x10000, v16
	v_and_b32_e32 v17, 0xffffff80, v12
	v_and_b32_e32 v18, 0xffffff80, v13
	v_and_b32_e32 v21, 0x7f, v77
	v_and_b32_e32 v20, 0x7f, v76
	v_and_b32_e32 v13, 0x7f, v13
	v_and_b32_e32 v12, 0x7f, v12
	v_and_b32_e32 v26, 0xffffff80, v14
	v_and_b32_e32 v28, 0xffffff80, v15
	v_and_b32_e32 v23, 0x7f, v79
	v_and_b32_e32 v22, 0x7f, v78
	v_and_b32_e32 v15, 0x7f, v15
	v_and_b32_e32 v14, 0x7f, v14
	ds_write_b128 v16, v[20:23]
	ds_write_b128 v16, v[12:15] offset:64
	v_and_b32_e32 v21, 0xffffff80, v8
	v_and_b32_e32 v23, 0xffffff80, v9
	v_and_b32_e32 v13, 0x7f, v73
	v_and_b32_e32 v12, 0x7f, v72
	v_and_b32_e32 v9, 0x7f, v9
	v_and_b32_e32 v8, 0x7f, v8
	v_and_b32_e32 v30, 0xffffff80, v10
	v_and_b32_e32 v32, 0xffffff80, v11
	v_and_b32_e32 v15, 0x7f, v75
	v_and_b32_e32 v14, 0x7f, v74
	v_and_b32_e32 v11, 0x7f, v11
	v_and_b32_e32 v10, 0x7f, v10
	v_and_b32_e32 v19, 0xffffff80, v76
	ds_write_b128 v16, v[12:15] offset:16
	ds_write_b128 v16, v[8:11] offset:80
	v_and_b32_e32 v13, 0xffffff80, v4
	v_and_b32_e32 v15, 0xffffff80, v5
	v_and_b32_e32 v9, 0x7f, v69
	v_and_b32_e32 v8, 0x7f, v68
	v_and_b32_e32 v5, 0x7f, v5
	v_and_b32_e32 v4, 0x7f, v4
	v_and_b32_e32 v34, 0xffffff80, v6
	v_and_b32_e32 v36, 0xffffff80, v7
	v_and_b32_e32 v11, 0x7f, v71
	v_and_b32_e32 v10, 0x7f, v70
	v_and_b32_e32 v7, 0x7f, v7
	v_and_b32_e32 v6, 0x7f, v6
	ds_write_b128 v16, v[8:11] offset:32
	ds_write_b128 v16, v[4:7] offset:96
	v_and_b32_e32 v5, 0x7f, v65
	v_and_b32_e32 v4, 0x7f, v64
	v_and_b32_e32 v41, 0xffffff80, v2
	v_and_b32_e32 v42, 0xffffff80, v3
	v_and_b32_e32 v7, 0x7f, v67
	v_and_b32_e32 v6, 0x7f, v66
	v_and_b32_e32 v11, 0x7f, v3
	v_and_b32_e32 v10, 0x7f, v2
	v_add_f32_e32 v2, v19, v17
	s_movk_i32 s3, 0xff00
	v_add_f32_e32 v3, v19, v18
	v_and_b32_e32 v24, 0xffffff80, v77
	ds_write_b128 v16, v[4:7] offset:48
	v_and_b32_e32 v2, 0xffffff00, v2
	v_and_or_b32 v3, v3, s3, 1
	v_add_f32_e32 v4, v19, v26
	v_add_f32_e32 v5, v19, v28
	v_and_b32_e32 v40, 0xffffff80, v1
	v_and_b32_e32 v9, 0x7f, v1
	v_and_b32_e32 v8, 0x7f, v0
	v_and_or_b32 v4, v4, s3, 2
	v_and_or_b32 v5, v5, s3, 3
	v_add_f32_e32 v48, v24, v17
	v_add_f32_e32 v49, v24, v18
	ds_write_b128 v16, v[8:11] offset:112
	v_add_f32_e32 v6, v19, v21
	v_add_f32_e32 v7, v19, v23
	v_add_f32_e32 v11, v19, v15
	v_add_f32_e32 v15, v19, v36
	v_add_f32_e32 v36, v19, v40
	v_max_f32_e32 v40, v2, v3
	v_min_f32_e32 v2, v2, v3
	v_max_f32_e32 v3, v5, v5
	v_and_or_b32 v48, v48, s3, 16
	v_and_or_b32 v49, v49, s3, 17
	v_add_f32_e32 v50, v24, v26
	v_add_f32_e32 v51, v24, v28
	v_and_or_b32 v6, v6, s3, 4
	v_and_or_b32 v7, v7, s3, 5
	v_add_f32_e32 v8, v19, v30
	v_add_f32_e32 v9, v19, v32
	v_max_f32_e32 v5, v4, v3
	v_min_f32_e32 v3, v4, v3
	v_and_or_b32 v50, v50, s3, 18
	v_and_or_b32 v51, v51, s3, 19
	v_and_or_b32 v8, v8, s3, 6
	v_and_or_b32 v9, v9, s3, 7
	v_max_f32_e32 v4, v40, v5
	v_min_f32_e32 v5, v40, v5
	v_max_f32_e32 v40, v2, v3
	v_add_f32_e32 v52, v24, v21
	v_add_f32_e32 v23, v24, v23
	v_add_f32_e32 v30, v24, v30
	v_add_f32_e32 v24, v24, v32
	v_max_f32_e32 v58, v48, v49
	v_min_f32_e32 v48, v48, v49
	v_max_f32_e32 v49, v51, v51
	v_min_f32_e32 v2, v2, v3
	v_max_f32_e32 v3, v40, v5
	v_min_f32_e32 v5, v40, v5
	v_max_f32_e32 v40, v6, v7
	v_min_f32_e32 v6, v6, v7
	v_max_f32_e32 v7, v9, v9
	v_and_or_b32 v52, v52, s3, 20
	v_and_or_b32 v23, v23, s3, 21
	v_and_or_b32 v30, v30, s3, 22
	v_and_or_b32 v24, v24, s3, 23
	v_max_f32_e32 v51, v50, v49
	v_min_f32_e32 v49, v50, v49
	v_max_f32_e32 v9, v8, v7
	v_min_f32_e32 v7, v8, v7
	v_max_f32_e32 v50, v58, v51
	v_min_f32_e32 v51, v58, v51
	v_max_f32_e32 v58, v48, v49
	v_max_f32_e32 v8, v40, v9
	v_min_f32_e32 v9, v40, v9
	v_max_f32_e32 v40, v6, v7
	v_min_f32_e32 v48, v48, v49
	v_max_f32_e32 v49, v58, v51
	v_min_f32_e32 v51, v58, v51
	v_max_f32_e32 v58, v52, v23
	v_min_f32_e32 v23, v52, v23
	v_max_f32_e32 v52, v30, v24
	v_min_f32_e32 v24, v30, v24
	v_min_f32_e32 v6, v6, v7
	v_max_f32_e32 v7, v40, v9
	v_min_f32_e32 v9, v40, v9
	v_max_f32_e32 v30, v58, v52
	v_min_f32_e32 v52, v58, v52
	v_max_f32_e32 v58, v23, v24
	v_max_f32_e32 v40, v4, v8
	v_min_f32_e32 v4, v4, v8
	v_max_f32_e32 v8, v5, v9
	v_min_f32_e32 v23, v23, v24
	v_max_f32_e32 v24, v58, v52
	v_min_f32_e32 v52, v58, v52
	v_and_b32_e32 v25, 0xffffff80, v78
	v_add_f32_e32 v10, v19, v13
	v_min_f32_e32 v5, v5, v9
	v_max_f32_e32 v9, v8, v4
	v_min_f32_e32 v4, v8, v4
	v_max_f32_e32 v8, v3, v7
	v_min_f32_e32 v3, v3, v7
	v_max_f32_e32 v7, v2, v6
	v_max_f32_e32 v58, v50, v30
	v_min_f32_e32 v30, v50, v30
	v_max_f32_e32 v50, v51, v52
	v_and_or_b32 v10, v10, s3, 8
	v_and_or_b32 v11, v11, s3, 9
	v_add_f32_e32 v13, v19, v34
	v_min_f32_e32 v2, v2, v6
	v_max_f32_e32 v6, v7, v3
	v_min_f32_e32 v3, v7, v3
	v_add_f32_e32 v32, v25, v17
	v_add_f32_e32 v53, v25, v18
	v_min_f32_e32 v51, v51, v52
	v_max_f32_e32 v52, v50, v30
	v_min_f32_e32 v30, v50, v30
	v_max_f32_e32 v50, v49, v24
	v_min_f32_e32 v24, v49, v24
	v_max_f32_e32 v49, v48, v23
	v_and_or_b32 v13, v13, s3, 10
	v_and_or_b32 v15, v15, s3, 11
	v_max_f32_e32 v7, v8, v9
	v_min_f32_e32 v8, v8, v9
	v_max_f32_e32 v9, v6, v4
	v_min_f32_e32 v4, v6, v4
	v_max_f32_e32 v6, v3, v5
	v_min_f32_e32 v3, v3, v5
	v_max_f32_e32 v5, v11, v11
	v_and_or_b32 v32, v32, s3, 32
	v_and_or_b32 v53, v53, s3, 33
	v_add_f32_e32 v54, v25, v26
	v_add_f32_e32 v55, v25, v28
	v_min_f32_e32 v23, v48, v23
	v_max_f32_e32 v48, v49, v24
	v_min_f32_e32 v24, v49, v24
	v_and_b32_e32 v27, 0xffffff80, v79
	v_and_b32_e32 v38, 0xffffff80, v0
	v_max_f32_e32 v11, v10, v5
	v_min_f32_e32 v5, v10, v5
	v_max_f32_e32 v10, v15, v15
;     __device__ __forceinline__ void fused(f32x4 (&acc)[2][2][4][2], const Unit& u, int wr, int wc, int fr, int fq, PG8_LAS unsigned char* lds, int wid, int lane) const {
;     ...
;             { float cv[16]; cv[0] = __uint_as_float((__float_as_uint(v0[0] + v1[0]) & ~255u) | 0u); cv[1] = __uint_as_float((__float_as_uint(v0[0] + v1[1]) & ~255u) | 1u); cv[2] = __uint_as_float((__float_as_uint(v0[0] + v1[2]) & ~255u) | 2u); cv[3] = __uint_as_float((__float_as_uint(v0[0] + v1[3]) & ~255u) | 3u); cv[4] = __uint_as_float((__float_as_uint(v0[0] + v1[4]) & ~255u) | 4u); cv[5] = __uint_as_float((__float_as_uint(v0[0] + v1[5]) & ~255u) | 5u); cv[6] = __uint_as_float((__float_as_uint(v0[0] + v1[6]) & ~255u) | 6u); cv[7] = __uint_as_float((__float_as_uint(v0[0] + v1[7]) & ~255u) | 7u); cv[8] = __uint_as_float((__float_as_uint(v0[0] + v1[8]) & ~255u) | 8u); cv[9] = __uint_as_float((__float_as_uint(v0[0] + v1[9]) & ~255u) | 9u); cv[10] = __uint_as_float((__float_as_uint(v0[0] + v1[10]) & ~255u) | 10u); cv[11] = __uint_as_float((__float_as_uint(v0[0] + v1[11]) & ~255u) | 11u); cv[12] = __uint_as_float((__float_as_uint(v0[0] + v1[12]) & ~255u) | 12u); cv[13] = __uint_as_float((__float_as_uint(v0[0] + v1[13]) & ~255u) | 13u); cv[14] = __uint_as_float((__float_as_uint(v0[0] + v1[14]) & ~255u) | 14u); cv[15] = __uint_as_float((__float_as_uint(v0[0] + v1[15]) & ~255u) | 15u); sort16_desc(cv);
; #pragma unroll
;               for (int q = 0; q < 16; ++q) best[q] = cv[q]; }
	v_and_or_b32 v54, v54, s3, 34
	v_and_or_b32 v55, v55, s3, 35
	v_max_f32_e32 v49, v50, v52
	v_min_f32_e32 v50, v50, v52
	v_max_f32_e32 v52, v48, v30
	v_min_f32_e32 v30, v48, v30
	v_max_f32_e32 v48, v24, v51
	v_min_f32_e32 v24, v24, v51
	v_max_f32_e32 v51, v53, v53
	v_add_f32_e32 v34, v19, v38
	v_max_f32_e32 v15, v13, v10
	v_min_f32_e32 v10, v13, v10
	v_add_f32_e32 v21, v25, v21
	v_add_f32_e32 v25, v27, v17
	v_max_f32_e32 v53, v32, v51
	v_min_f32_e32 v32, v32, v51
	v_max_f32_e32 v51, v55, v55
	v_and_or_b32 v34, v34, s3, 12
	v_and_or_b32 v36, v36, s3, 13
	v_add_f32_e32 v38, v19, v41
	v_add_f32_e32 v19, v19, v42
	v_max_f32_e32 v13, v11, v15
	v_min_f32_e32 v11, v11, v15
	v_max_f32_e32 v15, v5, v10
	v_and_or_b32 v21, v21, s3, 36
	v_and_or_b32 v25, v25, s3, 48
	v_add_f32_e32 v56, v27, v18
	v_add_f32_e32 v57, v27, v26
	v_max_f32_e32 v55, v54, v51
	v_min_f32_e32 v51, v54, v51
	v_and_or_b32 v38, v38, s3, 14
	v_and_or_b32 v19, v19, s3, 15
	v_min_f32_e32 v5, v5, v10
	v_max_f32_e32 v10, v15, v11
	v_min_f32_e32 v11, v15, v11
	v_max_f32_e32 v15, v36, v36
	v_and_or_b32 v56, v56, s3, 49
	v_and_or_b32 v57, v57, s3, 50
	v_max_f32_e32 v54, v53, v55
	v_min_f32_e32 v53, v53, v55
	v_max_f32_e32 v55, v32, v51
	v_max_f32_e32 v36, v34, v15
	v_min_f32_e32 v15, v34, v15
	v_max_f32_e32 v34, v38, v38
	v_min_f32_e32 v32, v32, v51
	v_max_f32_e32 v51, v55, v53
	v_min_f32_e32 v53, v55, v53
	v_max_f32_e32 v55, v21, v25
	v_min_f32_e32 v21, v21, v25
	v_max_f32_e32 v25, v57, v57
	v_max_f32_e32 v38, v34, v19
	v_min_f32_e32 v19, v34, v19
	v_max_f32_e32 v57, v56, v25
	v_min_f32_e32 v25, v56, v25
	v_max_f32_e32 v34, v36, v38
	v_min_f32_e32 v36, v36, v38
	v_max_f32_e32 v38, v15, v19
	v_max_f32_e32 v56, v55, v57
	v_min_f32_e32 v55, v55, v57
	v_max_f32_e32 v57, v21, v25
	v_min_f32_e32 v15, v15, v19
	v_max_f32_e32 v19, v38, v36
	v_min_f32_e32 v36, v38, v36
	v_min_f32_e32 v21, v21, v25
	v_max_f32_e32 v25, v57, v55
	v_min_f32_e32 v55, v57, v55
	v_max_f32_e32 v38, v13, v34
	v_min_f32_e32 v13, v13, v34
	v_max_f32_e32 v34, v11, v36
	v_max_f32_e32 v57, v54, v56
	v_min_f32_e32 v54, v54, v56
	v_max_f32_e32 v56, v53, v55
	v_min_f32_e32 v11, v11, v36
	v_max_f32_e32 v36, v34, v13
	v_min_f32_e32 v13, v34, v13
	v_max_f32_e32 v34, v10, v19
	v_min_f32_e32 v10, v10, v19
	v_max_f32_e32 v19, v5, v15
	v_min_f32_e32 v53, v53, v55
	v_max_f32_e32 v55, v56, v54
	v_min_f32_e32 v54, v56, v54
	v_max_f32_e32 v56, v51, v25
	v_min_f32_e32 v25, v51, v25
	v_max_f32_e32 v51, v32, v21
	v_min_f32_e32 v5, v5, v15
	v_max_f32_e32 v15, v19, v10
	v_min_f32_e32 v21, v32, v21
	v_max_f32_e32 v32, v51, v25
	v_min_f32_e32 v10, v19, v10
	v_max_f32_e32 v19, v34, v36
	v_min_f32_e32 v34, v34, v36
	v_max_f32_e32 v36, v15, v13
	v_min_f32_e32 v13, v15, v13
	v_min_f32_e32 v25, v51, v25
	v_max_f32_e32 v51, v56, v55
	v_min_f32_e32 v55, v56, v55
	v_max_f32_e32 v56, v32, v54
	v_min_f32_e32 v32, v32, v54
	v_max_f32_e32 v15, v10, v11
	v_min_f32_e32 v10, v10, v11
	v_min_f32_e32 v11, v40, v38
	v_max_f32_e32 v41, v4, v13
	v_max_f32_e32 v54, v25, v53
	v_min_f32_e32 v25, v25, v53
	v_min_f32_e32 v53, v58, v57
	v_max_f32_e32 v59, v30, v32
	v_min_f32_e32 v4, v4, v13
	v_max_f32_e32 v13, v41, v11
	v_min_f32_e32 v11, v41, v11
	v_max_f32_e32 v41, v8, v34
	v_min_f32_e32 v8, v8, v34
	v_max_f32_e32 v34, v3, v10
	v_min_f32_e32 v30, v30, v32
	v_max_f32_e32 v32, v59, v53
	v_min_f32_e32 v53, v59, v53
	v_max_f32_e32 v59, v50, v55
	v_min_f32_e32 v50, v50, v55
	v_max_f32_e32 v55, v24, v25
	v_min_f32_e32 v3, v3, v10
	v_max_f32_e32 v10, v34, v8
	v_min_f32_e32 v8, v34, v8
	v_min_f32_e32 v24, v24, v25
	v_max_f32_e32 v25, v55, v50
	v_min_f32_e32 v50, v55, v50
	v_max_f32_e32 v34, v41, v13
	v_min_f32_e32 v13, v41, v13
	v_max_f32_e32 v41, v10, v11
	v_min_f32_e32 v10, v10, v11
	v_max_f32_e32 v11, v8, v4
	v_min_f32_e32 v4, v8, v4
	v_max_f32_e32 v8, v7, v19
	v_min_f32_e32 v7, v7, v19
	v_max_f32_e32 v19, v6, v15
	v_max_f32_e32 v55, v59, v32
	v_min_f32_e32 v32, v59, v32
	v_max_f32_e32 v59, v25, v53
	v_min_f32_e32 v25, v25, v53
	v_max_f32_e32 v53, v50, v30
	v_min_f32_e32 v30, v50, v30
	v_max_f32_e32 v50, v49, v51
	v_min_f32_e32 v49, v49, v51
	v_max_f32_e32 v51, v48, v54
	v_min_f32_e32 v6, v6, v15
	v_max_f32_e32 v15, v19, v7
	v_min_f32_e32 v7, v19, v7
	v_max_f32_e32 v19, v9, v36
	v_min_f32_e32 v9, v9, v36
	v_max_f32_e32 v36, v2, v5
	v_min_f32_e32 v48, v48, v54
	v_max_f32_e32 v54, v51, v49
	v_min_f32_e32 v49, v51, v49
	v_max_f32_e32 v51, v52, v56
	v_min_f32_e32 v52, v52, v56
	v_max_f32_e32 v56, v23, v21
	v_min_f32_e32 v2, v2, v5
	v_max_f32_e32 v5, v36, v9
	v_min_f32_e32 v9, v36, v9
	v_max_f32_e32 v36, v19, v15
	v_min_f32_e32 v21, v23, v21
	v_max_f32_e32 v23, v56, v52
	v_min_f32_e32 v52, v56, v52
	v_and_b32_e32 v20, 0xffffff80, v72
	v_min_f32_e32 v15, v19, v15
	v_max_f32_e32 v19, v5, v7
	v_min_f32_e32 v5, v5, v7
	v_max_f32_e32 v7, v9, v6
	v_min_f32_e32 v6, v9, v6
	v_min_f32_e32 v9, v8, v34
	v_min_f32_e32 v42, v36, v13
	v_max_f32_e32 v56, v51, v54
	v_min_f32_e32 v51, v51, v54
	v_max_f32_e32 v54, v23, v49
	v_min_f32_e32 v23, v23, v49
	v_max_f32_e32 v49, v52, v48
	v_min_f32_e32 v48, v52, v48
	v_and_b32_e32 v39, 0xffffff80, v65
	v_min_f32_e32 v65, v48, v24
	v_max3_f32 v9, v9, v48, v24
	v_max3_f32 v24, v42, v49, v30
	v_add_f32_e32 v27, v27, v28
	v_add_f32_e32 v28, v20, v17
	v_add_f32_e32 v42, v20, v18
	v_add_f32_e32 v20, v20, v26
	v_and_b32_e32 v22, 0xffffff80, v73
	v_and_or_b32 v27, v27, s3, 51
	v_and_or_b32 v28, v28, s3, 64
	v_and_b32_e32 v42, 0xffffff00, v42
	v_and_b32_e32 v20, 0xffffff00, v20
	v_and_b32_e32 v29, 0xffffff80, v74
	v_and_b32_e32 v31, 0xffffff80, v75
	v_and_b32_e32 v33, 0xffffff80, v70
	v_and_b32_e32 v35, 0xffffff80, v71
	v_and_b32_e32 v37, 0xffffff80, v64
;     __device__ __forceinline__ void fused(f32x4 (&acc)[2][2][4][2], const Unit& u, int wr, int wc, int fr, int fq, PG8_LAS unsigned char* lds, int wid, int lane) const {
;     ...
;             { float cv[16]; cv[0] = __uint_as_float((__float_as_uint(v0[1] + v1[0]) & ~255u) | 16u); cv[1] = __uint_as_float((__float_as_uint(v0[1] + v1[1]) & ~255u) | 17u); cv[2] = __uint_as_float((__float_as_uint(v0[1] + v1[2]) & ~255u) | 18u); cv[3] = __uint_as_float((__float_as_uint(v0[1] + v1[3]) & ~255u) | 19u); cv[4] = __uint_as_float((__float_as_uint(v0[1] + v1[4]) & ~255u) | 20u); cv[5] = __uint_as_float((__float_as_uint(v0[1] + v1[5]) & ~255u) | 21u); cv[6] = __uint_as_float((__float_as_uint(v0[1] + v1[6]) & ~255u) | 22u); cv[7] = __uint_as_float((__float_as_uint(v0[1] + v1[7]) & ~255u) | 23u); cv[8] = __uint_as_float((__float_as_uint(v0[2] + v1[0]) & ~255u) | 32u); cv[9] = __uint_as_float((__float_as_uint(v0[2] + v1[1]) & ~255u) | 33u); cv[10] = __uint_as_float((__float_as_uint(v0[2] + v1[2]) & ~255u) | 34u); cv[11] = __uint_as_float((__float_as_uint(v0[2] + v1[3]) & ~255u) | 35u); cv[12] = __uint_as_float((__float_as_uint(v0[2] + v1[4]) & ~255u) | 36u); cv[13] = __uint_as_float((__float_as_uint(v0[3] + v1[0]) & ~255u) | 48u); cv[14] = __uint_as_float((__float_as_uint(v0[3] + v1[1]) & ~255u) | 49u); cv[15] = __uint_as_float((__float_as_uint(v0[3] + v1[2]) & ~255u) | 50u); sort16_desc(cv); merge_top16(best, cv); }
	v_min_f32_e32 v43, v15, v41
	v_min_f32_e32 v44, v19, v10
	v_min_f32_e32 v62, v54, v25
	v_or_b32_e32 v42, 0x41, v42
	v_or_b32_e32 v20, 0x42, v20
	v_add_f32_e32 v26, v22, v17
	v_add_f32_e32 v22, v22, v18
	v_min_f32_e32 v63, v23, v53
	v_max3_f32 v23, v43, v23, v53
	v_max3_f32 v10, v19, v10, v62
	v_max3_f32 v19, v44, v54, v25
	v_and_b32_e32 v26, 0xffffff00, v26
	v_and_b32_e32 v22, 0xffffff00, v22
	v_add_f32_e32 v43, v29, v17
	v_add_f32_e32 v29, v29, v18
	v_add_f32_e32 v44, v31, v17
	v_add_f32_e32 v18, v31, v18
	v_add_f32_e32 v31, v33, v17
	v_add_f32_e32 v33, v35, v17
	v_add_f32_e32 v35, v37, v17
	v_add_f32_e32 v37, v39, v17
	v_max_f32_e32 v39, v27, v28
	v_min_f32_e32 v27, v27, v28
	v_max_f32_e32 v28, v42, v42
	v_or_b32_e32 v26, 0x50, v26
	v_or_b32_e32 v22, 0x51, v22
	v_and_b32_e32 v43, 0xffffff00, v43
	v_and_b32_e32 v29, 0xffffff00, v29
	v_max_f32_e32 v42, v28, v20
	v_min_f32_e32 v20, v28, v20
	v_or_b32_e32 v43, 0x60, v43
	v_or_b32_e32 v29, 0x61, v29
	v_max_f32_e32 v28, v39, v42
	v_min_f32_e32 v39, v39, v42
	v_max_f32_e32 v42, v27, v20
	v_min_f32_e32 v20, v27, v20
	v_max_f32_e32 v27, v42, v39
	v_min_f32_e32 v39, v42, v39
	v_max_f32_e32 v42, v26, v22
	v_min_f32_e32 v22, v26, v22
	v_max_f32_e32 v26, v29, v29
	v_max_f32_e32 v29, v43, v43
	v_max_f32_e32 v43, v29, v26
	v_min_f32_e32 v26, v29, v26
	v_max_f32_e32 v29, v42, v43
	v_min_f32_e32 v42, v42, v43
	v_max_f32_e32 v43, v22, v26
	v_and_b32_e32 v12, 0xffffff80, v68
	v_and_b32_e32 v14, 0xffffff80, v69
	v_min_f32_e32 v22, v22, v26
	v_max_f32_e32 v26, v43, v42
	v_min_f32_e32 v42, v43, v42
	v_add_f32_e32 v12, v12, v17
	v_add_f32_e32 v14, v14, v17
	v_max_f32_e32 v43, v28, v29
	v_min_f32_e32 v28, v28, v29
	v_max_f32_e32 v29, v39, v42
	v_and_b32_e32 v44, 0xffffff00, v44
	v_and_b32_e32 v18, 0xffffff00, v18
	v_and_b32_e32 v12, 0xffffff00, v12
	v_and_b32_e32 v14, 0xffffff00, v14
	v_min_f32_e32 v39, v39, v42
	v_max_f32_e32 v42, v29, v28
	v_min_f32_e32 v28, v29, v28
	v_max_f32_e32 v29, v27, v26
	v_min_f32_e32 v26, v27, v26
	v_max_f32_e32 v27, v20, v22
	v_or_b32_e32 v44, 0x70, v44
	v_or_b32_e32 v18, 0x71, v18
	v_or_b32_e32 v12, 0x80, v12
	v_or_b32_e32 v14, 0x90, v14
	v_min_f32_e32 v20, v20, v22
	v_max_f32_e32 v22, v27, v26
	v_min_f32_e32 v26, v27, v26
	v_and_b32_e32 v31, 0xffffff00, v31
	v_and_b32_e32 v33, 0xffffff00, v33
	v_max_f32_e32 v27, v29, v42
	v_min_f32_e32 v29, v29, v42
	v_max_f32_e32 v42, v22, v28
	v_min_f32_e32 v22, v22, v28
	v_max_f32_e32 v28, v26, v39
	v_min_f32_e32 v26, v26, v39
	v_max_f32_e32 v39, v44, v44
	v_or_b32_e32 v31, 0xa0, v31
	v_or_b32_e32 v33, 0xb0, v33
	v_and_b32_e32 v35, 0xffffff00, v35
	v_and_b32_e32 v37, 0xffffff00, v37
	v_max_f32_e32 v44, v39, v18
	v_min_f32_e32 v18, v39, v18
	v_max_f32_e32 v39, v12, v14
	v_min_f32_e32 v12, v12, v14
	v_or_b32_e32 v35, 0xc0, v35
	v_or_b32_e32 v37, 0xd0, v37
	v_max_f32_e32 v14, v44, v39
	v_min_f32_e32 v39, v44, v39
	v_max_f32_e32 v44, v18, v12
	v_min_f32_e32 v12, v18, v12
	v_max_f32_e32 v18, v44, v39
	v_min_f32_e32 v39, v44, v39
	v_max_f32_e32 v44, v31, v33
	v_min_f32_e32 v31, v31, v33
	v_max_f32_e32 v33, v37, v37
	v_max_f32_e32 v37, v35, v33
	v_min_f32_e32 v33, v35, v33
	v_max_f32_e32 v35, v44, v37
	v_min_f32_e32 v37, v44, v37
	v_max_f32_e32 v44, v31, v33
	v_min_f32_e32 v31, v31, v33
	v_max_f32_e32 v33, v44, v37
	v_min_f32_e32 v37, v44, v37
	v_max_f32_e32 v44, v14, v35
	v_min_f32_e32 v14, v14, v35
	v_max_f32_e32 v35, v39, v37
	v_min_f32_e32 v37, v39, v37
	v_max_f32_e32 v39, v35, v14
	v_min_f32_e32 v14, v35, v14
	v_max_f32_e32 v35, v18, v33
	v_min_f32_e32 v18, v18, v33
	v_max_f32_e32 v33, v12, v31
	v_min_f32_e32 v12, v12, v31
	v_max_f32_e32 v31, v33, v18
	v_min_f32_e32 v45, v5, v11
	v_min_f32_e32 v61, v51, v59
	v_min_f32_e32 v18, v33, v18
	v_max_f32_e32 v33, v35, v39
	v_min_f32_e32 v35, v35, v39
	v_max_f32_e32 v39, v31, v14
	v_min_f32_e32 v14, v31, v14
	v_max3_f32 v5, v5, v11, v61
	v_max3_f32 v11, v45, v51, v59
	v_max_f32_e32 v31, v18, v37
	v_min_f32_e32 v18, v18, v37
	v_min_f32_e32 v37, v43, v44
	v_max_f32_e32 v45, v22, v14
	v_min_f32_e32 v14, v22, v14
	v_max_f32_e32 v22, v45, v37
	v_min_f32_e32 v37, v45, v37
	v_max_f32_e32 v45, v29, v35
	v_min_f32_e32 v29, v29, v35
	v_max_f32_e32 v35, v26, v18
	v_min_f32_e32 v46, v7, v4
	v_min_f32_e32 v47, v6, v3
	v_min_f32_e32 v52, v50, v55
	v_min_f32_e32 v60, v56, v32
	v_min_f32_e32 v64, v49, v30
	v_min_f32_e32 v18, v26, v18
	v_max_f32_e32 v26, v35, v29
	v_min_f32_e32 v29, v35, v29
	v_max3_f32 v21, v40, v38, v21
	v_max3_f32 v8, v8, v34, v65
	v_max3_f32 v13, v36, v13, v64
	v_max3_f32 v15, v15, v41, v63
	v_max3_f32 v4, v7, v4, v60
	v_max3_f32 v7, v46, v56, v32
	v_max3_f32 v3, v6, v3, v52
	v_max3_f32 v6, v47, v50, v55
	v_max3_f32 v2, v2, v58, v57
	v_max_f32_e32 v35, v45, v22
	v_min_f32_e32 v22, v45, v22
	v_max_f32_e32 v45, v26, v37
	v_min_f32_e32 v26, v26, v37
	v_max_f32_e32 v37, v29, v14
	v_min_f32_e32 v14, v29, v14
	v_max_f32_e32 v29, v27, v33
	v_min_f32_e32 v27, v27, v33
	v_max_f32_e32 v33, v28, v31
	v_max_f32_e32 v25, v21, v19
	v_min_f32_e32 v19, v21, v19
	v_max_f32_e32 v21, v8, v5
	v_min_f32_e32 v5, v8, v5
	v_max_f32_e32 v8, v9, v11
	v_min_f32_e32 v9, v9, v11
	v_max_f32_e32 v11, v13, v4
	v_min_f32_e32 v4, v13, v4
	v_max_f32_e32 v13, v24, v7
	v_min_f32_e32 v7, v24, v7
	v_max_f32_e32 v24, v15, v3
	v_min_f32_e32 v3, v15, v3
	v_max_f32_e32 v15, v23, v6
	v_min_f32_e32 v6, v23, v6
	v_max_f32_e32 v23, v10, v2
	v_min_f32_e32 v2, v10, v2
	v_min_f32_e32 v28, v28, v31
	v_max_f32_e32 v31, v33, v27
	v_min_f32_e32 v27, v33, v27
	v_max_f32_e32 v33, v42, v39
	v_min_f32_e32 v39, v42, v39
	v_max_f32_e32 v42, v20, v12
	v_max_f32_e32 v10, v25, v13
	v_min_f32_e32 v13, v25, v13
	v_max_f32_e32 v25, v21, v24
	v_min_f32_e32 v21, v21, v24
; __device__ __forceinline__ void merge_top16(float (&v)[16], const float (&nw)[16]) {
;     v[0] = fmaxf(v[0], nw[15]); v[1] = fmaxf(v[1], nw[14]); v[2] = fmaxf(v[2], nw[13]); v[3] = fmaxf(v[3], nw[12]); v[4] = fmaxf(v[4], nw[11]); v[5] = fmaxf(v[5], nw[10]); v[6] = fmaxf(v[6], nw[9]); v[7] = fmaxf(v[7], nw[8]); v[8] = fmaxf(v[8], nw[7]); v[9] = fmaxf(v[9], nw[6]); v[10] = fmaxf(v[10], nw[5]); v[11] = fmaxf(v[11], nw[4]); v[12] = fmaxf(v[12], nw[3]); v[13] = fmaxf(v[13], nw[2]); v[14] = fmaxf(v[14], nw[1]); v[15] = fmaxf(v[15], nw[0]);
;     CE(v[0], v[8]); CE(v[1], v[9]); CE(v[2], v[10]); CE(v[3], v[11]);
;     CE(v[4], v[12]); CE(v[5], v[13]); CE(v[6], v[14]); CE(v[7], v[15]);
;     CE(v[0], v[4]); CE(v[1], v[5]); CE(v[2], v[6]); CE(v[3], v[7]);
;     CE(v[8], v[12]); CE(v[9], v[13]); CE(v[10], v[14]); CE(v[11], v[15]);
;     CE(v[0], v[2]); CE(v[1], v[3]); CE(v[4], v[6]); CE(v[5], v[7]);
;     CE(v[8], v[10]); CE(v[9], v[11]); CE(v[12], v[14]); CE(v[13], v[15]);
;     __device__ __forceinline__ void fused(f32x4 (&acc)[2][2][4][2], const Unit& u, int wr, int wc, int fr, int fq, PG8_LAS unsigned char* lds, int wid, int lane) const {
;     ...
;             { float cv[16]; cv[0] = __uint_as_float((__float_as_uint(v0[14] + v1[0]) & ~255u) | 224u); cv[1] = __uint_as_float((__float_as_uint(v0[15] + v1[0]) & ~255u) | 240u); cv[2] = -INFINITY; cv[3] = -INFINITY; cv[4] = -INFINITY; cv[5] = -INFINITY; cv[6] = -INFINITY; cv[7] = -INFINITY; cv[8] = -INFINITY; cv[9] = -INFINITY; cv[10] = -INFINITY; cv[11] = -INFINITY; cv[12] = -INFINITY; cv[13] = -INFINITY; cv[14] = -INFINITY; cv[15] = -INFINITY; sort16_desc(cv); merge_top16(best, cv); }
;             float sc[16], sum = 0.f;
; #pragma unroll
;             for (int q = 0; q < 16; ++q) { sc[q] = __uint_as_float(__float_as_uint(best[q]) & ~255u); }
;             const float smax = sc[0];
; #pragma unroll
;             for (int q = 0; q < 16; ++q) { sc[q] = __builtin_amdgcn_exp2f((sc[q] - smax) * 1.4426950408889634f); }
; #pragma unroll
;             for (int q = 0; q < 16; ++q) sum += sc[q];
;             const float rs = 1.0f / sum;
;             asm volatile("s_waitcnt lgkmcnt(0)" ::: "memory");
;             int ex[16];
; #pragma unroll
;             for (int q = 0; q < 16; ++q) { const unsigned cid = __float_as_uint(best[q]) & 255u; ex[q] = idxl[cid >> 4] * 128 + idxl[16 + (cid & 15u)]; }
	v_max_f32_e32 v24, v8, v15
	v_min_f32_e32 v8, v8, v15
	v_max_f32_e32 v15, v11, v23
	v_min_f32_e32 v11, v11, v23
	v_max_f32_e32 v23, v19, v7
	v_min_f32_e32 v7, v19, v7
	v_max_f32_e32 v19, v5, v3
	v_min_f32_e32 v3, v5, v3
	v_max_f32_e32 v5, v9, v6
	v_min_f32_e32 v6, v9, v6
	v_max_f32_e32 v9, v4, v2
	v_min_f32_e32 v2, v4, v2
	v_min_f32_e32 v12, v20, v12
	v_max_f32_e32 v20, v42, v39
	v_min_f32_e32 v39, v42, v39
	v_and_b32_e32 v1, 0xffffff80, v66
	v_and_b32_e32 v0, 0xffffff80, v67
	v_max_f32_e32 v4, v10, v24
	v_min_f32_e32 v10, v10, v24
	v_max_f32_e32 v24, v25, v15
	v_min_f32_e32 v15, v25, v15
	v_max_f32_e32 v25, v13, v8
	v_min_f32_e32 v8, v13, v8
	v_max_f32_e32 v13, v21, v11
	v_min_f32_e32 v11, v21, v11
	v_max_f32_e32 v21, v23, v5
	v_min_f32_e32 v5, v23, v5
	v_max_f32_e32 v23, v19, v9
	v_min_f32_e32 v9, v19, v9
	v_max_f32_e32 v19, v7, v6
	v_min_f32_e32 v6, v7, v6
	v_max_f32_e32 v7, v3, v2
	v_min_f32_e32 v2, v3, v2
	v_max_f32_e32 v42, v33, v31
	v_min_f32_e32 v31, v33, v31
	v_max_f32_e32 v33, v20, v27
	v_min_f32_e32 v20, v20, v27
	v_max_f32_e32 v27, v39, v28
	v_min_f32_e32 v28, v39, v28
	v_min_f32_e32 v3, v4, v24
	v_min_f32_e32 v30, v10, v15
	v_min_f32_e32 v32, v25, v13
	v_min_f32_e32 v34, v8, v11
	v_min_f32_e32 v36, v21, v23
	v_min_f32_e32 v38, v5, v9
	v_min_f32_e32 v40, v19, v7
	v_min_f32_e32 v41, v6, v2
	v_max_f32_e32 v39, v29, v35
	v_min_f32_e32 v29, v29, v35
	v_max_f32_e32 v35, v42, v22
	v_min_f32_e32 v22, v42, v22
	v_max_f32_e32 v42, v31, v45
	v_min_f32_e32 v31, v31, v45
	v_max_f32_e32 v45, v33, v26
	v_min_f32_e32 v26, v33, v26
	v_max_f32_e32 v33, v20, v37
	v_min_f32_e32 v20, v20, v37
	v_max_f32_e32 v37, v27, v14
	v_min_f32_e32 v14, v27, v14
	v_max_f32_e32 v27, v28, v18
	v_min_f32_e32 v18, v28, v18
	v_add_f32_e32 v1, v1, v17
	v_add_f32_e32 v0, v0, v17
	v_max3_f32 v4, v4, v24, v12
	v_max_f32_e32 v3, v3, v18
	v_max3_f32 v10, v10, v15, v27
	v_max_f32_e32 v12, v30, v14
	v_max3_f32 v13, v25, v13, v37
	v_max_f32_e32 v14, v32, v20
	v_max3_f32 v8, v8, v11, v33
	v_max_f32_e32 v11, v34, v26
	v_max3_f32 v15, v21, v23, v45
	v_max_f32_e32 v18, v36, v31
	v_max3_f32 v5, v5, v9, v42
	v_max_f32_e32 v9, v38, v22
	v_max3_f32 v7, v19, v7, v35
	v_max_f32_e32 v19, v40, v29
	v_max3_f32 v2, v6, v2, v39
	v_max3_f32 v6, v41, v43, v44
	v_and_b32_e32 v1, 0xffffff00, v1
	v_and_b32_e32 v0, 0xffffff00, v0
	v_max_f32_e32 v20, v4, v15
	v_min_f32_e32 v4, v4, v15
	v_max_f32_e32 v15, v3, v18
	v_min_f32_e32 v3, v3, v18
	v_max_f32_e32 v18, v10, v5
	v_min_f32_e32 v5, v10, v5
	v_max_f32_e32 v10, v12, v9
	v_min_f32_e32 v9, v12, v9
	v_max_f32_e32 v12, v13, v7
	v_min_f32_e32 v7, v13, v7
	v_max_f32_e32 v13, v14, v19
	v_min_f32_e32 v14, v14, v19
	v_max_f32_e32 v19, v8, v2
	v_min_f32_e32 v2, v8, v2
	v_max_f32_e32 v8, v11, v6
	v_min_f32_e32 v6, v11, v6
	v_or_b32_e32 v1, 0xe0, v1
	v_or_b32_e32 v0, 0xf0, v0
	v_max_f32_e32 v11, v20, v12
	v_min_f32_e32 v12, v20, v12
	v_max_f32_e32 v20, v15, v13
	v_min_f32_e32 v13, v15, v13
	v_max_f32_e32 v15, v18, v19
	v_min_f32_e32 v18, v18, v19
	v_max_f32_e32 v19, v10, v8
	v_min_f32_e32 v8, v10, v8
	v_max_f32_e32 v10, v4, v7
	v_min_f32_e32 v4, v4, v7
	v_max_f32_e32 v7, v3, v14
	v_min_f32_e32 v3, v3, v14
	v_max_f32_e32 v14, v5, v2
	v_min_f32_e32 v2, v5, v2
	v_max_f32_e32 v5, v9, v6
	v_min_f32_e32 v6, v9, v6
	v_max_f32_e32 v9, v11, v15
	v_min_f32_e32 v11, v11, v15
	v_max_f32_e32 v15, v20, v19
	v_min_f32_e32 v19, v20, v19
	v_max_f32_e32 v20, v12, v18
	v_min_f32_e32 v12, v12, v18
	v_max_f32_e32 v18, v13, v8
	v_min_f32_e32 v8, v13, v8
	v_max_f32_e32 v13, v10, v14
	v_min_f32_e32 v10, v10, v14
	v_max_f32_e32 v14, v7, v5
	v_min_f32_e32 v5, v7, v5
	v_max_f32_e32 v7, v4, v2
	v_min_f32_e32 v2, v4, v2
	v_max_f32_e32 v4, v3, v6
	v_min_f32_e32 v3, v3, v6
	v_max_f32_e32 v17, v1, v0
	v_min_f32_e32 v0, v1, v0
	v_min_f32_e32 v6, v9, v15
	v_min_f32_e32 v21, v11, v19
	v_min_f32_e32 v22, v20, v18
	v_min_f32_e32 v23, v12, v8
	v_min_f32_e32 v24, v13, v14
	v_min_f32_e32 v25, v10, v5
	v_min_f32_e32 v26, v7, v4
	v_min_f32_e32 v27, v2, v3
	s_mov_b32 s3, 0xff800000
	v_max_f32_e32 v0, 0xff800000, v0
	v_max3_f32 v1, v9, v15, s3
	v_max_f32_e32 v6, 0xff800000, v6
	v_max3_f32 v9, v11, v19, s3
	v_max_f32_e32 v11, 0xff800000, v21
	v_max3_f32 v15, v20, v18, s3
	v_max_f32_e32 v18, 0xff800000, v22
	v_max3_f32 v8, v12, v8, s3
	v_max_f32_e32 v12, 0xff800000, v23
	v_max3_f32 v13, v13, v14, s3
	v_max_f32_e32 v14, 0xff800000, v24
	v_max3_f32 v5, v10, v5, s3
	v_max_f32_e32 v10, 0xff800000, v25
	v_max3_f32 v4, v7, v4, s3
	v_max_f32_e32 v7, 0xff800000, v26
	v_max3_f32 v0, v2, v3, v0
	v_max3_f32 v2, v27, v17, s3
	v_max_f32_e32 v3, v1, v13
	v_min_f32_e32 v1, v1, v13
	v_max_f32_e32 v13, v6, v14
	v_min_f32_e32 v6, v6, v14
	v_max_f32_e32 v14, v9, v5
	v_min_f32_e32 v5, v9, v5
	v_max_f32_e32 v9, v11, v10
	v_min_f32_e32 v10, v11, v10
	v_max_f32_e32 v11, v15, v4
	v_min_f32_e32 v4, v15, v4
	v_max_f32_e32 v15, v18, v7
	v_max_f32_e32 v17, v8, v0
	v_min_f32_e32 v0, v8, v0
	v_max_f32_e32 v8, v12, v2
	v_min_f32_e32 v2, v12, v2
	v_max_f32_e32 v12, v3, v11
	v_min_f32_e32 v3, v3, v11
	v_max_f32_e32 v11, v13, v15
	v_min_f32_e32 v13, v13, v15
	v_max_f32_e32 v15, v14, v17
	v_min_f32_e32 v14, v14, v17
	v_max_f32_e32 v17, v9, v8
	v_min_f32_e32 v8, v9, v8
	v_max_f32_e32 v9, v1, v4
	v_min_f32_e32 v24, v1, v4
	v_max_f32_e32 v27, v5, v0
	v_min_f32_e32 v28, v5, v0
	v_max_f32_e32 v29, v10, v2
	v_min_f32_e32 v30, v10, v2
	v_max_f32_e32 v0, v12, v15
	v_min_f32_e32 v1, v12, v15
	v_max_f32_e32 v2, v11, v17
	v_min_f32_e32 v4, v11, v17
	v_min_f32_e32 v7, v18, v7
	v_max_f32_e32 v33, v0, v2
	v_min_f32_e32 v34, v0, v2
	v_min_f32_e32 v36, v1, v4
	v_max_f32_e32 v25, v6, v7
	v_min_f32_e32 v26, v6, v7
	v_max_f32_e32 v35, v1, v4
	v_lshrrev_b32_e32 v0, 2, v33
	v_lshrrev_b32_e32 v2, 2, v34
	v_lshrrev_b32_e32 v6, 2, v36
	v_max_f32_e32 v17, v3, v14
	v_min_f32_e32 v31, v3, v14
	v_and_b32_e32 v0, 60, v0
	v_and_b32_e32 v1, 15, v33
	v_and_b32_e32 v2, 60, v2
	v_and_b32_e32 v3, 15, v34
	v_lshrrev_b32_e32 v4, 2, v35
	v_and_b32_e32 v5, 15, v35
	v_and_b32_e32 v6, 60, v6
	v_and_b32_e32 v7, 15, v36
	s_waitcnt lgkmcnt(0)
; #define RT_PK(q_) (ex[q_] | (int)((__float_as_uint(usc[ex[q_]]) >> 23) << 14))
;     __device__ __forceinline__ void fused(f32x4 (&acc)[2][2][4][2], const Unit& u, int wr, int wc, int fr, int fq, PG8_LAS unsigned char* lds, int wid, int lane) const {
;     ...
;             float sc[16], sum = 0.f;
; #pragma unroll
;             for (int q = 0; q < 16; ++q) { sc[q] = __uint_as_float(__float_as_uint(best[q]) & ~255u); }
;             const float smax = sc[0];
; #pragma unroll
;             for (int q = 0; q < 16; ++q) { sc[q] = __builtin_amdgcn_exp2f((sc[q] - smax) * 1.4426950408889634f); }
; #pragma unroll
;             for (int q = 0; q < 16; ++q) sum += sc[q];
;             const float rs = 1.0f / sum;
;             asm volatile("s_waitcnt lgkmcnt(0)" ::: "memory");
;             int ex[16];
; #pragma unroll
;             for (int q = 0; q < 16; ++q) { const unsigned cid = __float_as_uint(best[q]) & 255u; ex[q] = idxl[cid >> 4] * 128 + idxl[16 + (cid & 15u)]; }
;             const size_t o = ((size_t)u.pn * 16384 + (size_t)(u.pm * BM + row)) * 16;
;             typedef int i32x4 __attribute__((ext_vector_type(4)));
; #pragma unroll
;             for (int i = 0; i < 4; ++i) {
;     ...
;                 *(i32x4*)(eidx + o + 4 * i) = (i32x4){RT_PK(4 * i), RT_PK(4 * i + 1), RT_PK(4 * i + 2), RT_PK(4 * i + 3)};
;                 *(f32x4*)(egate + o + 4 * i) = (f32x4){sc[4 * i] * rs * vsc[ex[4 * i]], sc[4 * i + 1] * rs * vsc[ex[4 * i + 1]], sc[4 * i + 2] * rs * vsc[ex[4 * i + 2]], sc[4 * i + 3] * rs * vsc[ex[4 * i + 3]]};
	v_add_u32_e32 v0, v16, v0
	v_lshl_add_u32 v1, v1, 2, v16
	v_add_u32_e32 v2, v16, v2
	v_lshl_add_u32 v3, v3, 2, v16
	v_and_b32_e32 v4, 60, v4
	v_lshl_add_u32 v5, v5, 2, v16
	v_add_u32_e32 v6, v16, v6
	v_lshl_add_u32 v7, v7, 2, v16
	v_add_u32_e32 v4, v16, v4
	ds_read_b32 v0, v0
	ds_read_b32 v1, v1 offset:64
	ds_read_b32 v2, v2
	ds_read_b32 v3, v3 offset:64
	ds_read_b32 v10, v4
	ds_read_b32 v5, v5 offset:64
	ds_read_b32 v6, v6
	ds_read_b32 v7, v7 offset:64
	s_waitcnt lgkmcnt(0)
	v_lshl_add_u32 v0, v0, 7, v1
	v_ashrrev_i32_e32 v1, 31, v0
	v_lshl_add_u32 v4, v2, 7, v3
	v_lshlrev_b64 v[14:15], 3, v[0:1]
	v_lshl_add_u32 v10, v10, 7, v5
	v_lshl_add_u32 v12, v6, 7, v7
	v_lshl_add_u64 v[2:3], s[8:9], 0, v[14:15]
	v_ashrrev_i32_e32 v5, 31, v4
	v_max_f32_e32 v32, v13, v8
	v_min_f32_e32 v8, v13, v8
	global_load_dwordx2 v[170:171], v[2:3], off
	v_lshlrev_b64 v[18:19], 3, v[4:5]
	v_ashrrev_i32_e32 v11, 31, v10
	v_ashrrev_i32_e32 v13, 31, v12
	v_lshl_add_u64 v[2:3], s[8:9], 0, v[18:19]
	v_lshlrev_b64 v[20:21], 3, v[10:11]
	v_lshlrev_b64 v[22:23], 3, v[12:13]
	v_lshl_add_u64 v[6:7], s[8:9], 0, v[20:21]
	global_load_dwordx2 v[172:173], v[2:3], off
	global_load_dwordx2 v[174:175], v[6:7], off
	v_lshl_add_u64 v[2:3], s[8:9], 0, v[22:23]
	global_load_dwordx2 v[176:177], v[2:3], off
	v_min_f32_e32 v2, v9, v27
	v_min_f32_e32 v6, v25, v29
	v_max_f32_e32 v43, v2, v6
	v_min_f32_e32 v44, v2, v6
	v_and_b32_e32 v2, 0xffffff00, v34
	v_and_b32_e32 v51, 0xffffff00, v33
	v_max_f32_e32 v37, v9, v27
	v_max_f32_e32 v3, v25, v29
	v_sub_f32_e32 v2, v2, v51
	v_min_f32_e32 v9, v24, v28
	v_min_f32_e32 v25, v26, v30
	v_max_f32_e32 v41, v37, v3
	v_min_f32_e32 v42, v37, v3
	v_and_b32_e32 v3, 0xffffff00, v35
	v_mul_f32_e32 v2, 0x3fb8aa3b, v2
	v_max_f32_e32 v47, v9, v25
	v_min_f32_e32 v48, v9, v25
	v_exp_f32_e32 v25, v2
	v_sub_f32_e32 v2, v3, v51
	v_and_b32_e32 v6, 0xffffff00, v36
	v_mul_f32_e32 v2, 0x3fb8aa3b, v2
	v_max_f32_e32 v7, v24, v28
	v_max_f32_e32 v24, v26, v30
	v_max_f32_e32 v38, v17, v32
	v_exp_f32_e32 v26, v2
	v_sub_f32_e32 v2, v6, v51
	v_max_f32_e32 v45, v7, v24
	v_min_f32_e32 v46, v7, v24
	v_and_b32_e32 v7, 0xffffff00, v38
	v_mul_f32_e32 v2, 0x3fb8aa3b, v2
	v_min_f32_e32 v17, v17, v32
	v_exp_f32_e32 v27, v2
	v_sub_f32_e32 v2, v7, v51
	v_max_f32_e32 v39, v31, v8
	v_min_f32_e32 v40, v31, v8
	v_and_b32_e32 v8, 0xffffff00, v17
	v_mul_f32_e32 v2, 0x3fb8aa3b, v2
	v_exp_f32_e32 v28, v2
	v_sub_f32_e32 v2, v8, v51
	v_and_b32_e32 v9, 0xffffff00, v39
	v_mul_f32_e32 v2, 0x3fb8aa3b, v2
	v_exp_f32_e32 v29, v2
	v_sub_f32_e32 v2, v9, v51
	v_and_b32_e32 v31, 0xffffff00, v40
	v_mul_f32_e32 v2, 0x3fb8aa3b, v2
	v_exp_f32_e32 v30, v2
	v_sub_f32_e32 v2, v31, v51
	v_and_b32_e32 v32, 0xffffff00, v41
	v_mul_f32_e32 v2, 0x3fb8aa3b, v2
	v_exp_f32_e32 v31, v2
	v_sub_f32_e32 v2, v32, v51
	v_and_b32_e32 v34, 0xffffff00, v42
	v_mul_f32_e32 v2, 0x3fb8aa3b, v2
	v_exp_f32_e32 v6, v2
	v_sub_f32_e32 v2, v34, v51
	v_and_b32_e32 v35, 0xffffff00, v43
	v_mul_f32_e32 v2, 0x3fb8aa3b, v2
	v_exp_f32_e32 v7, v2
	v_sub_f32_e32 v2, v35, v51
	v_mul_f32_e32 v2, 0x3fb8aa3b, v2
	v_exp_f32_e32 v8, v2
	v_lshl_or_b32 v2, s18, 8, v128
	v_ashrrev_i32_e32 v3, 31, v2
	s_lshl_b64 s[4:5], s[16:17], 18
	s_mov_b32 s3, 0x7fc000
	v_lshl_add_u64 v[32:33], v[2:3], 4, s[4:5]
	v_sub_f32_e32 v24, v51, v51
	v_mul_f32_e32 v24, 0x3fb8aa3b, v24
	v_exp_f32_e32 v24, v24
	s_waitcnt vmcnt(0)
	v_lshrrev_b32_e32 v1, 9, v170
	v_and_or_b32 v2, v1, s3, v0
	v_and_b32_e32 v36, 0xffffff00, v44
	v_and_b32_e32 v37, 0xffffff00, v45
	v_and_b32_e32 v49, 0xffffff00, v46
	v_and_b32_e32 v50, 0xffffff00, v47
	v_and_b32_e32 v52, 0xffffff00, v48
	v_lshrrev_b32_e32 v0, 9, v172
	v_and_or_b32 v3, v0, s3, v4
	v_lshrrev_b32_e32 v0, 9, v174
	v_and_or_b32 v4, v0, s3, v10
	v_lshrrev_b32_e32 v0, 9, v176
	v_and_or_b32 v5, v0, s3, v12
	v_lshlrev_b64 v[12:13], 2, v[32:33]
	v_lshl_add_u64 v[0:1], s[12:13], 0, v[12:13]
	s_nop 0
	v_readfirstlane_b32 s98, v0
	v_readfirstlane_b32 s99, v1
	v_lshrrev_b32_e32 v202, 6, v128
	v_and_b32_e32 v203, 63, v128
	v_lshlrev_b32_e32 v202, 13, v202
	v_lshl_or_b32 v204, v203, 6, v202
	v_lshl_or_b32 v205, v203, 4, v202
	v_lshlrev_b32_e32 v203, 4, v203
	ds_write_b128 v204, v[2:5]
	v_lshrrev_b32_e32 v32, 2, v40
	v_add_f32_e32 v10, 0, v24
	v_add_f32_e32 v10, v25, v10
	v_add_f32_e32 v10, v26, v10
	v_add_f32_e32 v10, v27, v10
	v_sub_f32_e32 v2, v36, v51
	v_add_f32_e32 v10, v28, v10
	v_mul_f32_e32 v2, 0x3fb8aa3b, v2
	v_add_f32_e32 v10, v29, v10
	v_exp_f32_e32 v9, v2
	v_sub_f32_e32 v2, v37, v51
	v_add_f32_e32 v10, v30, v10
	v_mul_f32_e32 v2, 0x3fb8aa3b, v2
	v_sub_f32_e32 v3, v49, v51
	v_add_f32_e32 v10, v31, v10
	v_exp_f32_e32 v2, v2
	v_mul_f32_e32 v3, 0x3fb8aa3b, v3
	v_sub_f32_e32 v4, v50, v51
	v_add_f32_e32 v10, v6, v10
	v_exp_f32_e32 v3, v3
	v_mul_f32_e32 v4, 0x3fb8aa3b, v4
	v_sub_f32_e32 v5, v52, v51
	v_add_f32_e32 v10, v7, v10
	v_exp_f32_e32 v4, v4
	v_mul_f32_e32 v5, 0x3fb8aa3b, v5
	v_add_f32_e32 v10, v8, v10
	v_exp_f32_e32 v5, v5
	v_add_f32_e32 v10, v9, v10
	v_add_f32_e32 v10, v2, v10
	v_lshrrev_b32_e32 v11, 2, v38
	v_lshrrev_b32_e32 v15, 2, v17
	v_add_f32_e32 v10, v3, v10
	v_and_b32_e32 v11, 60, v11
	v_and_b32_e32 v14, 15, v38
	v_and_b32_e32 v15, 60, v15
	v_and_b32_e32 v17, 15, v17
	v_lshrrev_b32_e32 v22, 2, v39
	v_and_b32_e32 v23, 15, v39
	v_and_b32_e32 v33, 15, v40
	v_add_f32_e32 v10, v4, v10
	v_add_u32_e32 v11, v16, v11
	v_lshl_add_u32 v14, v14, 2, v16
	v_add_u32_e32 v15, v16, v15
	v_lshl_add_u32 v17, v17, 2, v16
	v_and_b32_e32 v22, 60, v22
	v_lshl_add_u32 v23, v23, 2, v16
	v_and_b32_e32 v32, 60, v32
	v_lshl_add_u32 v33, v33, 2, v16
	v_add_f32_e32 v10, v5, v10
	v_add_u32_e32 v22, v16, v22
	v_add_u32_e32 v32, v16, v32
	ds_read_b32 v11, v11
	ds_read_b32 v14, v14 offset:64
	ds_read_b32 v15, v15
	ds_read_b32 v17, v17 offset:64
	ds_read_b32 v34, v22
	ds_read_b32 v23, v23 offset:64
	ds_read_b32 v35, v32
	ds_read_b32 v33, v33 offset:64
	s_waitcnt lgkmcnt(6)
; #define RT_PK(q_) (ex[q_] | (int)((__float_as_uint(usc[ex[q_]]) >> 23) << 14))
;     __device__ __forceinline__ void fused(f32x4 (&acc)[2][2][4][2], const Unit& u, int wr, int wc, int fr, int fq, PG8_LAS unsigned char* lds, int wid, int lane) const {
;     ...
;             const float rs = 1.0f / sum;
;             asm volatile("s_waitcnt lgkmcnt(0)" ::: "memory");
;             int ex[16];
; #pragma unroll
;             for (int q = 0; q < 16; ++q) { const unsigned cid = __float_as_uint(best[q]) & 255u; ex[q] = idxl[cid >> 4] * 128 + idxl[16 + (cid & 15u)]; }
;             const size_t o = ((size_t)u.pn * 16384 + (size_t)(u.pm * BM + row)) * 16;
;             typedef int i32x4 __attribute__((ext_vector_type(4)));
; #pragma unroll
;             for (int i = 0; i < 4; ++i) {
;     ...
;                 *(i32x4*)(eidx + o + 4 * i) = (i32x4){RT_PK(4 * i), RT_PK(4 * i + 1), RT_PK(4 * i + 2), RT_PK(4 * i + 3)};
;                 *(f32x4*)(egate + o + 4 * i) = (f32x4){sc[4 * i] * rs * vsc[ex[4 * i]], sc[4 * i + 1] * rs * vsc[ex[4 * i + 1]], sc[4 * i + 2] * rs * vsc[ex[4 * i + 2]], sc[4 * i + 3] * rs * vsc[ex[4 * i + 3]]};
;             }
	v_lshl_add_u32 v14, v11, 7, v14
	v_div_scale_f32 v11, s[4:5], v10, v10, 1.0
	v_rcp_f32_e32 v36, v11
	s_waitcnt lgkmcnt(4)
	v_lshl_add_u32 v22, v15, 7, v17
	s_waitcnt lgkmcnt(2)
	v_lshl_add_u32 v32, v34, 7, v23
	s_waitcnt lgkmcnt(0)
	v_lshl_add_u32 v34, v35, 7, v33
	v_fma_f32 v15, -v11, v36, 1.0
	v_fmac_f32_e32 v36, v15, v36
	v_div_scale_f32 v15, vcc, 1.0, v10, 1.0
	v_mul_f32_e32 v17, v15, v36
	v_fma_f32 v23, -v11, v17, v15
	v_fmac_f32_e32 v17, v23, v36
	v_fma_f32 v11, -v11, v17, v15
	v_div_fmas_f32 v11, v11, v36, v17
	v_div_fixup_f32 v10, v11, v10, 1.0
	v_pk_mul_f32 v[24:25], v[24:25], v[10:11] op_sel_hi:[1,0]
	v_pk_mul_f32 v[26:27], v[26:27], v[10:11] op_sel_hi:[1,0]
	v_ashrrev_i32_e32 v15, 31, v14
	v_ashrrev_i32_e32 v33, 31, v32
	v_lshl_add_u64 v[12:13], s[10:11], 0, v[12:13]
	s_nop 0
	v_readfirstlane_b32 s100, v12
	v_readfirstlane_b32 s101, v13
	v_ashrrev_i32_e32 v23, 31, v22
	v_lshlrev_b64 v[36:37], 3, v[32:33]
	v_lshl_add_u64 v[38:39], s[8:9], 0, v[36:37]
	v_ashrrev_i32_e32 v35, 31, v34
	v_mul_f32_e32 v18, v24, v171
	v_mul_f32_e32 v19, v25, v173
	v_lshlrev_b64 v[24:25], 3, v[14:15]
	v_mul_f32_e32 v20, v26, v175
	v_mul_f32_e32 v21, v27, v177
	ds_write_b128 v204, v[18:21] offset:4096
	v_lshlrev_b64 v[26:27], 3, v[22:23]
	s_nop 0
	v_lshl_add_u64 v[18:19], s[8:9], 0, v[24:25]
	v_lshl_add_u64 v[20:21], s[8:9], 0, v[26:27]
	global_load_dwordx2 v[178:179], v[18:19], off
	global_load_dwordx2 v[180:181], v[20:21], off
	global_load_dwordx2 v[182:183], v[38:39], off
	v_lshlrev_b64 v[38:39], 3, v[34:35]
	v_lshl_add_u64 v[18:19], s[8:9], 0, v[38:39]
	global_load_dwordx2 v[184:185], v[18:19], off
	s_waitcnt vmcnt(3)
	v_lshrrev_b32_e32 v11, 9, v178
	v_and_or_b32 v18, v11, s3, v14
	s_waitcnt vmcnt(2)
	v_lshrrev_b32_e32 v11, 9, v180
	v_and_or_b32 v19, v11, s3, v22
	s_waitcnt vmcnt(1)
	v_lshrrev_b32_e32 v11, 9, v182
	v_and_or_b32 v20, v11, s3, v32
	s_waitcnt vmcnt(0)
	v_lshrrev_b32_e32 v11, 9, v184
	v_and_or_b32 v21, v11, s3, v34
	ds_write_b128 v204, v[18:21] offset:16
	v_lshrrev_b32_e32 v11, 2, v41
	v_lshrrev_b32_e32 v15, 2, v42
	v_lshrrev_b32_e32 v18, 2, v43
	v_lshrrev_b32_e32 v20, 2, v44
	v_and_b32_e32 v11, 60, v11
	v_and_b32_e32 v14, 15, v41
	v_and_b32_e32 v15, 60, v15
	v_and_b32_e32 v17, 15, v42
	v_and_b32_e32 v18, 60, v18
	v_and_b32_e32 v19, 15, v43
	v_and_b32_e32 v20, 60, v20
	v_and_b32_e32 v21, 15, v44
	v_add_u32_e32 v11, v16, v11
	v_lshl_add_u32 v14, v14, 2, v16
	v_add_u32_e32 v15, v16, v15
	v_lshl_add_u32 v17, v17, 2, v16
	v_add_u32_e32 v18, v16, v18
	v_lshl_add_u32 v19, v19, 2, v16
	v_add_u32_e32 v20, v16, v20
	v_lshl_add_u32 v21, v21, 2, v16
	ds_read_b32 v11, v11
	ds_read_b32 v14, v14 offset:64
	ds_read_b32 v15, v15
	ds_read_b32 v17, v17 offset:64
	ds_read_b32 v18, v18
	ds_read_b32 v19, v19 offset:64
	ds_read_b32 v20, v20
	ds_read_b32 v21, v21 offset:64
	s_waitcnt lgkmcnt(6)
	v_lshl_add_u32 v14, v11, 7, v14
	s_waitcnt lgkmcnt(4)
	v_lshl_add_u32 v22, v15, 7, v17
	s_waitcnt lgkmcnt(2)
	v_lshl_add_u32 v32, v18, 7, v19
	v_pk_mul_f32 v[18:19], v[28:29], v[10:11] op_sel_hi:[1,0]
	s_waitcnt lgkmcnt(0)
	v_lshl_add_u32 v34, v20, 7, v21
	v_pk_mul_f32 v[20:21], v[30:31], v[10:11] op_sel_hi:[1,0]
	v_ashrrev_i32_e32 v15, 31, v14
	v_ashrrev_i32_e32 v33, 31, v32
	v_ashrrev_i32_e32 v23, 31, v22
	v_lshlrev_b64 v[28:29], 3, v[32:33]
	v_lshl_add_u64 v[30:31], s[8:9], 0, v[28:29]
	v_ashrrev_i32_e32 v35, 31, v34
	v_mul_f32_e32 v20, v20, v183
	v_mul_f32_e32 v21, v21, v185
	v_mul_f32_e32 v18, v18, v179
	v_mul_f32_e32 v19, v19, v181
	v_lshlrev_b64 v[24:25], 3, v[14:15]
	ds_write_b128 v204, v[18:21] offset:4112
	v_lshlrev_b64 v[26:27], 3, v[22:23]
	s_nop 0
	v_lshl_add_u64 v[18:19], s[8:9], 0, v[24:25]
	v_lshl_add_u64 v[20:21], s[8:9], 0, v[26:27]
	global_load_dwordx2 v[186:187], v[18:19], off
	global_load_dwordx2 v[188:189], v[20:21], off
	global_load_dwordx2 v[190:191], v[30:31], off
	v_lshlrev_b64 v[30:31], 3, v[34:35]
	v_lshl_add_u64 v[18:19], s[8:9], 0, v[30:31]
	global_load_dwordx2 v[192:193], v[18:19], off
	s_waitcnt vmcnt(3)
; #define RT_PK(q_) (ex[q_] | (int)((__float_as_uint(usc[ex[q_]]) >> 23) << 14))
;     __device__ __forceinline__ void fused(f32x4 (&acc)[2][2][4][2], const Unit& u, int wr, int wc, int fr, int fq, PG8_LAS unsigned char* lds, int wid, int lane) const {
;     ...
;             for (int q = 0; q < 16; ++q) { const unsigned cid = __float_as_uint(best[q]) & 255u; ex[q] = idxl[cid >> 4] * 128 + idxl[16 + (cid & 15u)]; }
;             const size_t o = ((size_t)u.pn * 16384 + (size_t)(u.pm * BM + row)) * 16;
;             typedef int i32x4 __attribute__((ext_vector_type(4)));
; #pragma unroll
;             for (int i = 0; i < 4; ++i) {
;     ...
;                 *(i32x4*)(eidx + o + 4 * i) = (i32x4){RT_PK(4 * i), RT_PK(4 * i + 1), RT_PK(4 * i + 2), RT_PK(4 * i + 3)};
;                 *(f32x4*)(egate + o + 4 * i) = (f32x4){sc[4 * i] * rs * vsc[ex[4 * i]], sc[4 * i + 1] * rs * vsc[ex[4 * i + 1]], sc[4 * i + 2] * rs * vsc[ex[4 * i + 2]], sc[4 * i + 3] * rs * vsc[ex[4 * i + 3]]};
;             }
	v_lshrrev_b32_e32 v11, 9, v186
	v_and_or_b32 v18, v11, s3, v14
	s_waitcnt vmcnt(2)
	v_lshrrev_b32_e32 v11, 9, v188
	v_and_or_b32 v19, v11, s3, v22
	s_waitcnt vmcnt(1)
	v_lshrrev_b32_e32 v11, 9, v190
	v_and_or_b32 v20, v11, s3, v32
	s_waitcnt vmcnt(0)
	v_lshrrev_b32_e32 v11, 9, v192
	v_and_or_b32 v21, v11, s3, v34
	ds_write_b128 v204, v[18:21] offset:32
	v_lshrrev_b32_e32 v11, 2, v45
	v_lshrrev_b32_e32 v15, 2, v46
	v_lshrrev_b32_e32 v18, 2, v47
	v_lshrrev_b32_e32 v20, 2, v48
	v_and_b32_e32 v11, 60, v11
	v_and_b32_e32 v14, 15, v45
	v_and_b32_e32 v15, 60, v15
	v_and_b32_e32 v17, 15, v46
	v_and_b32_e32 v18, 60, v18
	v_and_b32_e32 v19, 15, v47
	v_and_b32_e32 v20, 60, v20
	v_add_u32_e32 v11, v16, v11
	v_lshl_add_u32 v14, v14, 2, v16
	v_add_u32_e32 v15, v16, v15
	v_lshl_add_u32 v17, v17, 2, v16
	v_add_u32_e32 v18, v16, v18
	v_lshl_add_u32 v19, v19, 2, v16
	v_add_u32_e32 v20, v16, v20
	v_and_b32_e32 v21, 15, v48
	v_lshl_add_u32 v16, v21, 2, v16
	ds_read_b32 v11, v11
	ds_read_b32 v14, v14 offset:64
	ds_read_b32 v15, v15
	ds_read_b32 v17, v17 offset:64
	ds_read_b32 v18, v18
	ds_read_b32 v19, v19 offset:64
	ds_read_b32 v20, v20
	ds_read_b32 v21, v16 offset:64
	s_waitcnt lgkmcnt(6)
	v_lshl_add_u32 v14, v11, 7, v14
	s_waitcnt lgkmcnt(4)
	v_lshl_add_u32 v16, v15, 7, v17
	s_waitcnt lgkmcnt(2)
	v_lshl_add_u32 v18, v18, 7, v19
	v_pk_mul_f32 v[6:7], v[6:7], v[10:11] op_sel_hi:[1,0]
	v_pk_mul_f32 v[8:9], v[8:9], v[10:11] op_sel_hi:[1,0]
	v_ashrrev_i32_e32 v15, 31, v14
	v_ashrrev_i32_e32 v19, 31, v18
	s_waitcnt lgkmcnt(0)
	v_lshl_add_u32 v20, v20, 7, v21
	v_lshlrev_b64 v[22:23], 3, v[14:15]
	v_ashrrev_i32_e32 v17, 31, v16
	v_ashrrev_i32_e32 v21, 31, v20
	v_mul_f32_e32 v8, v8, v191
	v_mul_f32_e32 v9, v9, v193
	v_mul_f32_e32 v6, v6, v187
	v_mul_f32_e32 v7, v7, v189
	v_lshlrev_b64 v[26:27], 3, v[18:19]
	ds_write_b128 v204, v[6:9] offset:4128
	v_lshlrev_b64 v[24:25], 3, v[16:17]
	v_lshl_add_u64 v[28:29], s[8:9], 0, v[26:27]
	v_lshl_add_u64 v[6:7], s[8:9], 0, v[22:23]
	v_lshl_add_u64 v[8:9], s[8:9], 0, v[24:25]
	global_load_dwordx2 v[194:195], v[6:7], off
	global_load_dwordx2 v[196:197], v[8:9], off
	global_load_dwordx2 v[198:199], v[28:29], off
	v_lshlrev_b64 v[28:29], 3, v[20:21]
	v_lshl_add_u64 v[6:7], s[8:9], 0, v[28:29]
	global_load_dwordx2 v[200:201], v[6:7], off
	s_waitcnt vmcnt(3)
	v_lshrrev_b32_e32 v6, 9, v194
	s_waitcnt vmcnt(2)
	v_lshrrev_b32_e32 v7, 9, v196
	s_waitcnt vmcnt(1)
	v_lshrrev_b32_e32 v8, 9, v198
	v_and_or_b32 v6, v6, s3, v14
	v_and_or_b32 v7, v7, s3, v16
	s_waitcnt vmcnt(0)
	v_lshrrev_b32_e32 v9, 9, v200
	v_and_or_b32 v8, v8, s3, v18
	v_and_or_b32 v9, v9, s3, v20
	ds_write_b128 v204, v[6:9] offset:48
	v_pk_mul_f32 v[0:1], v[2:3], v[10:11] op_sel_hi:[1,0]
	v_pk_mul_f32 v[2:3], v[4:5], v[10:11] op_sel_hi:[1,0]
	v_mul_f32_e32 v0, v0, v195
	v_mul_f32_e32 v1, v1, v197
	v_mul_f32_e32 v2, v2, v199
	v_mul_f32_e32 v3, v3, v201
	ds_write_b128 v204, v[0:3] offset:4144
	s_waitcnt lgkmcnt(0)
	ds_read_b128 v[140:143], v205
	ds_read_b128 v[144:147], v205 offset:1024
	ds_read_b128 v[148:151], v205 offset:2048
	ds_read_b128 v[152:155], v205 offset:3072
	ds_read_b128 v[156:159], v205 offset:4096
	ds_read_b128 v[160:163], v205 offset:5120
	ds_read_b128 v[164:167], v205 offset:6144
	ds_read_b128 v[206:209], v205 offset:7168
	s_waitcnt lgkmcnt(0)
	global_store_dwordx4 v203, v[140:143], s[98:99]
	global_store_dwordx4 v203, v[144:147], s[98:99] offset:1024
	global_store_dwordx4 v203, v[148:151], s[98:99] offset:2048
	global_store_dwordx4 v203, v[152:155], s[98:99] offset:3072
	global_store_dwordx4 v203, v[156:159], s[100:101]
	global_store_dwordx4 v203, v[160:163], s[100:101] offset:1024
	global_store_dwordx4 v203, v[164:167], s[100:101] offset:2048
	global_store_dwordx4 v203, v[206:209], s[100:101] offset:3072
